# speedup vs baseline: 1.0231x; 1.0132x over previous
_Z16closed_form_mainPKfS0_PKiPf:
	s_load_dwordx8 s[16:23], s[0:1], 0x0
	s_lshr_b32 s6, s2, 3
	v_readfirstlane_b32 s0, v0
	s_mul_hi_u32 s7, s6, 0x24924925
	s_lshr_b32 s4, s0, 6
	s_and_b32 s0, s2, 7
	s_mul_i32 s1, s7, 7
	s_mov_b32 s5, 0
	s_sub_i32 s1, s6, s1
	s_mul_i32 s36, s0, 7
	s_xor_b32 s3, s4, s5
	s_add_i32 s36, s36, s1
	s_waitcnt lgkmcnt(0)
	s_mov_b64 s[28:29], s[22:23]
	v_and_b32_e32 v19, 63, v0
	s_cmp_lt_u32 s36, 52
	s_mov_b64 s[0:1], -1
	s_cbranch_scc0 .LBB0_32
	s_mul_hi_u32 s0, s6, 0x20820821
	s_lshr_b32 s38, s0, 3
	s_mul_hi_u32 s0, s7, 0x1c71c71d
	s_mul_i32 s0, s0, 9
	s_sub_i32 s0, s7, s0
	v_add_u32_e32 v2, -3, v19
	v_mad_u64_u32 v[0:1], s[0:1], s0, 57, v[2:3]
	s_mov_b64 s[24:25], s[18:19]
	v_mov_b32_e32 v1, 0x200
	v_med3_i32 v1, v0, 0, v1
	s_mul_i32 s34, s36, 10
	s_and_b32 s17, s17, 0xffff
	s_and_b32 s25, s25, 0xffff
	v_cmp_gt_u32_e64 s[0:1], 57, v2
	s_mov_b32 s19, 0x20000
	s_mov_b32 s18, 0xe0e038
	s_mov_b32 s26, 0x606018
	s_mul_i32 s35, s38, 0x70701c
	s_mul_i32 s33, s38, 0x30300c
	v_lshlrev_b32_e32 v28, 2, v1
	v_mul_u32_u24_e32 v27, 12, v1
	v_lshlrev_b32_e32 v23, 4, v19
	s_cmp_lg_u32 s4, s5
	v_sub_u32_e64 v29, s34, 2 clamp
	s_cbranch_scc0 .LBB0_15
	s_setprio 2
	s_mov_b32 s27, s19
	s_and_b32 s21, s21, 0xffff
	s_mov_b32 s22, 0x202008
	s_mov_b32 s23, s19
	s_mul_i32 s38, s38, 0x101004
	s_movk_i32 s37, 0x80
	v_add_u32_e32 v18, -1, v0
	s_movk_i32 s4, 0x201
	s_movk_i32 s5, 0x1ff
	v_cmp_gt_u32_e64 s[40:41], s4, v0
	v_cmp_gt_u32_e64 s[42:43], s5, v18
	v_mov_b32_e32 v18, 0x42c80000
	v_mov_b32_e32 v22, 0x3de38e39
	v_mov_b32_e32 v26, 0x3a3d6628
	v_mov_b32_e32 v1, 0
	s_add_i32 s4, s34, -3
	s_max_i32 s4, s4, 0
	s_mul_i32 s4, s4, 0x804
	s_add_i32 s4, s4, s38
	buffer_load_dword v29, v28, s[20:23], s4 offen nt
	s_add_i32 s4, s34, -2
	s_max_i32 s4, s4, 0
	s_mul_i32 s4, s4, 0x804
	s_add_i32 s4, s4, s38
	buffer_load_dword v2, v28, s[20:23], s4 offen nt
	s_add_i32 s5, s34, -2
	s_max_i32 s5, s5, 0
	s_mul_i32 s6, s5, 0x804
	s_add_i32 s6, s6, s35
	s_add_i32 s7, s6, 0x505014
	s_add_i32 s8, s6, 0x606018
	s_mul_i32 s9, s5, 0x180c
	s_add_i32 s9, s9, s33
	s_add_i32 s4, s34, -1
	s_max_i32 s4, s4, 0
	s_mul_i32 s4, s4, 0x804
	s_add_i32 s4, s4, s38
	buffer_load_dword v3, v28, s[20:23], s4 offen nt
	buffer_load_dwordx3 v[8:10], v27, s[24:27], s9 offen nt
	buffer_load_dword v4, v28, s[16:19], s7 offen nt
	buffer_load_dword v5, v28, s[16:19], s8 offen nt
	s_add_i32 s5, s34, -1
	s_max_i32 s5, s5, 0
	s_mul_i32 s6, s5, 0x804
	s_add_i32 s6, s6, s35
	s_add_i32 s7, s6, 0x505014
	s_add_i32 s8, s6, 0x606018
	s_mul_i32 s9, s5, 0x180c
	s_add_i32 s9, s9, s33
	s_add_i32 s4, s34, 0
	s_min_i32 s4, s4, 0x200
	s_mul_i32 s4, s4, 0x804
	s_add_i32 s4, s4, s38
	buffer_load_dword v16, v28, s[20:23], s4 offen nt
	buffer_load_dwordx3 v[12:14], v27, s[24:27], s9 offen nt
	buffer_load_dword v6, v28, s[16:19], s7 offen nt
	buffer_load_dword v7, v28, s[16:19], s8 offen nt
	s_add_i32 s5, s34, 0
	s_min_i32 s5, s5, 0x200
	s_mul_i32 s6, s5, 0x804
	s_add_i32 s6, s6, s35
	s_add_i32 s7, s6, 0x505014
	s_add_i32 s8, s6, 0x606018
	s_mul_i32 s9, s5, 0x180c
	s_add_i32 s9, s9, s33
	s_add_i32 s4, s34, 1
	s_min_i32 s4, s4, 0x200
	s_mul_i32 s4, s4, 0x804
	s_add_i32 s4, s4, s38
	buffer_load_dword v17, v28, s[20:23], s4 offen nt
	buffer_load_dwordx3 v[32:34], v27, s[24:27], s9 offen nt
	buffer_load_dword v20, v28, s[16:19], s7 offen nt
	buffer_load_dword v21, v28, s[16:19], s8 offen nt
	s_waitcnt vmcnt(12)
	s_add_i32 s4, s34, -3
	s_cmpk_lt_u32 s4, 0x201
	s_cselect_b64 s[12:13], s[40:41], 0
	v_cmp_eq_u32_e64 s[14:15], s37, v29
	s_and_b64 s[14:15], s[14:15], s[12:13]
	v_cndmask_b32_e64 v24, 0, 1, s[14:15]
	s_add_i32 s4, s34, -2
	s_cmpk_lt_u32 s4, 0x201
	s_cselect_b64 s[12:13], s[40:41], 0
	v_cmp_eq_u32_e64 s[14:15], s37, v2
	s_and_b64 s[14:15], s[14:15], s[12:13]
	v_cndmask_b32_e64 v25, 0, 1, s[14:15]
	s_nop 0
	v_or_b32_dpp v30, v24, v24 wave_shr:1 row_mask:0xf bank_mask:0xf bound_ctrl:1
	v_or_b32_dpp v31, v25, v25 wave_shr:1 row_mask:0xf bank_mask:0xf bound_ctrl:1
	s_nop 1
	v_or_b32_dpp v30, v24, v30 wave_shl:1 row_mask:0xf bank_mask:0xf bound_ctrl:1
	v_or_b32_dpp v31, v25, v31 wave_shl:1 row_mask:0xf bank_mask:0xf bound_ctrl:1
	s_nop 1
	v_or_b32_dpp v36, v30, v30 wave_shr:1 row_mask:0xf bank_mask:0xf bound_ctrl:1
	v_or_b32_dpp v37, v31, v31 wave_shr:1 row_mask:0xf bank_mask:0xf bound_ctrl:1
	s_nop 1
	v_or_b32_dpp v36, v30, v36 wave_shl:1 row_mask:0xf bank_mask:0xf bound_ctrl:1
	v_or_b32_dpp v37, v31, v37 wave_shl:1 row_mask:0xf bank_mask:0xf bound_ctrl:1
	v_mov_b32_e32 v24, 0
	v_mov_b32_e32 v25, 0
	s_waitcnt vmcnt(8)
	v_mov_b32_dpp v40, v8 wave_shr:1 row_mask:0xf bank_mask:0xf bound_ctrl:1
	v_mov_b32_dpp v41, v9 wave_shr:1 row_mask:0xf bank_mask:0xf bound_ctrl:1
	v_mov_b32_dpp v42, v10 wave_shr:1 row_mask:0xf bank_mask:0xf bound_ctrl:1
	v_mov_b32_dpp v44, v8 wave_shl:1 row_mask:0xf bank_mask:0xf bound_ctrl:1
	v_mov_b32_dpp v45, v9 wave_shl:1 row_mask:0xf bank_mask:0xf bound_ctrl:1
	v_mov_b32_dpp v46, v10 wave_shl:1 row_mask:0xf bank_mask:0xf bound_ctrl:1
	s_add_i32 s4, s34, -1
	s_cmpk_lt_u32 s4, 0x201
	s_cselect_b64 s[12:13], s[40:41], 0
	v_cmp_eq_u32_e64 s[14:15], s37, v3
	s_and_b64 s[14:15], s[14:15], s[12:13]
	v_cndmask_b32_e64 v30, 0, 1, s[14:15]
	v_pk_add_f32 v[38:39], v[8:9], v[40:41]
	v_pk_mul_f32 v[48:49], v[8:9], v[8:9] op_sel_hi:[0,1]
	v_or_b32_dpp v31, v30, v30 wave_shr:1 row_mask:0xf bank_mask:0xf bound_ctrl:1
	v_pk_mul_f32 v[50:51], v[8:9], v[10:11] op_sel_hi:[1,0]
	v_or_b32_dpp v31, v30, v31 wave_shl:1 row_mask:0xf bank_mask:0xf bound_ctrl:1
	v_mul_f32_e64 v52, v9, v9
	v_mul_f32_e64 v53, v10, v10
	v_or_b32_dpp v56, v31, v31 wave_shr:1 row_mask:0xf bank_mask:0xf bound_ctrl:1
	v_add_f32_e64 v54, v10, v42
	v_pk_add_f32 v[38:39], v[38:39], v[44:45]
	v_or_b32_dpp v56, v31, v56 wave_shl:1 row_mask:0xf bank_mask:0xf bound_ctrl:1
	v_or3_b32 v57, v56, v37, v36
	v_or3_b32 v57, v57, v24, v25
	s_add_i32 s4, s34, -4
	s_cmpk_lt_u32 s4, 0x1ff
	s_cselect_b64 s[12:13], s[42:43], 0
	v_cmp_ne_u32_e64 s[30:31], 0, v57
	s_and_b64 s[30:31], s[30:31], s[12:13]
	v_cndmask_b32_e64 v57, 0, 1.0, s[30:31]
	v_pk_fma_f32 v[48:49], v[40:41], v[40:41], v[48:49] op_sel_hi:[0,1,1]
	v_pk_fma_f32 v[50:51], v[40:41], v[42:43], v[50:51] op_sel_hi:[1,0,1]
	v_fma_f32 v52, v41, v41, v52
	v_fma_f32 v53, v42, v42, v53
	v_add_f32_dpp v55, v57, v57 wave_shr:1 row_mask:0xf bank_mask:0xf bound_ctrl:1
	v_add_f32_e64 v54, v54, v46
	v_pk_fma_f32 v[48:49], v[44:45], v[44:45], v[48:49] op_sel_hi:[0,1,1]
	v_pk_fma_f32 v[50:51], v[44:45], v[46:47], v[50:51] op_sel_hi:[1,0,1]
	v_fma_f32 v52, v45, v45, v52
	v_fma_f32 v53, v46, v46, v53
	v_add_f32_dpp v55, v57, v55 wave_shl:1 row_mask:0xf bank_mask:0xf bound_ctrl:1
	v_mov_b32_dpp v30, v4 wave_shr:1 row_mask:0xf bank_mask:0xf bound_ctrl:1
	v_mov_b32_dpp v31, v5 wave_shr:1 row_mask:0xf bank_mask:0xf bound_ctrl:1
	v_mov_b32_dpp v58, v4 wave_shl:1 row_mask:0xf bank_mask:0xf bound_ctrl:1
	v_mov_b32_dpp v59, v5 wave_shl:1 row_mask:0xf bank_mask:0xf bound_ctrl:1
	v_pk_mul_f32 v[60:61], v[4:5], v[8:9] op_sel_hi:[1,0]
	v_pk_mul_f32 v[64:65], v[4:5], v[8:9] op_sel:[0,1]
	v_pk_mul_f32 v[68:69], v[4:5], v[10:11] op_sel_hi:[1,0]
	v_pk_add_f32 v[72:73], v[4:5], v[30:31]
	v_pk_fma_f32 v[60:61], v[30:31], v[40:41], v[60:61] op_sel_hi:[1,0,1]
	v_pk_fma_f32 v[64:65], v[30:31], v[40:41], v[64:65] op_sel:[0,1,0]
	v_pk_fma_f32 v[68:69], v[30:31], v[42:43], v[68:69] op_sel_hi:[1,0,1]
	v_pk_add_f32 v[72:73], v[72:73], v[58:59]
	v_pk_fma_f32 v[60:61], v[58:59], v[44:45], v[60:61] op_sel_hi:[1,0,1]
	v_pk_fma_f32 v[64:65], v[58:59], v[44:45], v[64:65] op_sel:[0,1,0]
	v_pk_fma_f32 v[68:69], v[58:59], v[46:47], v[68:69] op_sel_hi:[1,0,1]
	s_barrier
	s_add_i32 s5, s34, 1
	s_min_i32 s5, s5, 0x200
	s_mul_i32 s6, s5, 0x804
	s_add_i32 s6, s6, s35
	s_add_i32 s7, s6, 0x505014
	s_add_i32 s8, s6, 0x606018
	s_mul_i32 s9, s5, 0x180c
	s_add_i32 s9, s9, s33
	s_add_i32 s4, s34, 2
	s_min_i32 s4, s4, 0x200
	s_mul_i32 s4, s4, 0x804
	s_add_i32 s4, s4, s38
	buffer_load_dword v25, v28, s[20:23], s4 offen nt
	buffer_load_dwordx3 v[76:78], v27, s[24:27], s9 offen nt
	buffer_load_dword v30, v28, s[16:19], s7 offen nt
	buffer_load_dword v31, v28, s[16:19], s8 offen nt
	s_waitcnt vmcnt(8)
	v_mov_b32_dpp v80, v12 wave_shr:1 row_mask:0xf bank_mask:0xf bound_ctrl:1
	v_mov_b32_dpp v81, v13 wave_shr:1 row_mask:0xf bank_mask:0xf bound_ctrl:1
	v_mov_b32_dpp v82, v14 wave_shr:1 row_mask:0xf bank_mask:0xf bound_ctrl:1
	v_mov_b32_dpp v84, v12 wave_shl:1 row_mask:0xf bank_mask:0xf bound_ctrl:1
	v_mov_b32_dpp v85, v13 wave_shl:1 row_mask:0xf bank_mask:0xf bound_ctrl:1
	v_mov_b32_dpp v86, v14 wave_shl:1 row_mask:0xf bank_mask:0xf bound_ctrl:1
	s_add_i32 s4, s34, 0
	s_cmpk_lt_u32 s4, 0x201
	s_cselect_b64 s[12:13], s[40:41], 0
	v_cmp_eq_u32_e64 s[14:15], s37, v16
	s_and_b64 s[14:15], s[14:15], s[12:13]
	v_cndmask_b32_e64 v57, 0, 1, s[14:15]
	v_pk_add_f32 v[58:59], v[12:13], v[80:81]
	v_pk_mul_f32 v[62:63], v[12:13], v[12:13] op_sel_hi:[0,1]
	v_or_b32_dpp v88, v57, v57 wave_shr:1 row_mask:0xf bank_mask:0xf bound_ctrl:1
	v_pk_mul_f32 v[66:67], v[12:13], v[14:15] op_sel_hi:[1,0]
	v_or_b32_dpp v88, v57, v88 wave_shl:1 row_mask:0xf bank_mask:0xf bound_ctrl:1
	v_mul_f32_e64 v70, v13, v13
	v_mul_f32_e64 v71, v14, v14
	v_or_b32_dpp v89, v88, v88 wave_shr:1 row_mask:0xf bank_mask:0xf bound_ctrl:1
	v_add_f32_e64 v74, v14, v82
	v_pk_add_f32 v[58:59], v[58:59], v[84:85]
	v_or_b32_dpp v89, v88, v89 wave_shl:1 row_mask:0xf bank_mask:0xf bound_ctrl:1
	v_or3_b32 v57, v89, v56, v37
	v_or3_b32 v57, v57, v36, v24
	s_add_i32 s4, s34, -3
	s_cmpk_lt_u32 s4, 0x1ff
	s_cselect_b64 s[12:13], s[42:43], 0
	v_cmp_ne_u32_e64 s[30:31], 0, v57
	s_and_b64 s[30:31], s[30:31], s[12:13]
	v_cndmask_b32_e64 v57, 0, 1.0, s[30:31]
	v_pk_fma_f32 v[62:63], v[80:81], v[80:81], v[62:63] op_sel_hi:[0,1,1]
	v_pk_fma_f32 v[66:67], v[80:81], v[82:83], v[66:67] op_sel_hi:[1,0,1]
	v_fma_f32 v70, v81, v81, v70
	v_fma_f32 v71, v82, v82, v71
	v_add_f32_dpp v75, v57, v57 wave_shr:1 row_mask:0xf bank_mask:0xf bound_ctrl:1
	v_add_f32_e64 v74, v74, v86
	v_pk_fma_f32 v[62:63], v[84:85], v[84:85], v[62:63] op_sel_hi:[0,1,1]
	v_pk_fma_f32 v[66:67], v[84:85], v[86:87], v[66:67] op_sel_hi:[1,0,1]
	v_fma_f32 v70, v85, v85, v70
	v_fma_f32 v71, v86, v86, v71
	v_add_f32_dpp v75, v57, v75 wave_shl:1 row_mask:0xf bank_mask:0xf bound_ctrl:1
	v_mov_b32_dpp v92, v6 wave_shr:1 row_mask:0xf bank_mask:0xf bound_ctrl:1
	v_mov_b32_dpp v93, v7 wave_shr:1 row_mask:0xf bank_mask:0xf bound_ctrl:1
	v_mov_b32_dpp v96, v6 wave_shl:1 row_mask:0xf bank_mask:0xf bound_ctrl:1
	v_mov_b32_dpp v97, v7 wave_shl:1 row_mask:0xf bank_mask:0xf bound_ctrl:1
	v_pk_mul_f32 v[90:91], v[6:7], v[12:13] op_sel_hi:[1,0]
	v_pk_mul_f32 v[94:95], v[6:7], v[12:13] op_sel:[0,1]
	v_pk_mul_f32 v[98:99], v[6:7], v[14:15] op_sel_hi:[1,0]
	v_pk_add_f32 v[102:103], v[6:7], v[92:93]
	v_pk_fma_f32 v[90:91], v[92:93], v[80:81], v[90:91] op_sel_hi:[1,0,1]
	v_pk_fma_f32 v[94:95], v[92:93], v[80:81], v[94:95] op_sel:[0,1,0]
	v_pk_fma_f32 v[98:99], v[92:93], v[82:83], v[98:99] op_sel_hi:[1,0,1]
	v_pk_add_f32 v[102:103], v[102:103], v[96:97]
	v_pk_fma_f32 v[90:91], v[96:97], v[84:85], v[90:91] op_sel_hi:[1,0,1]
	v_pk_fma_f32 v[94:95], v[96:97], v[84:85], v[94:95] op_sel:[0,1,0]
	v_pk_fma_f32 v[98:99], v[96:97], v[86:87], v[98:99] op_sel_hi:[1,0,1]
	s_barrier
	s_add_i32 s5, s34, 2
	s_min_i32 s5, s5, 0x200
	s_mul_i32 s6, s5, 0x804
	s_add_i32 s6, s6, s35
	s_add_i32 s7, s6, 0x505014
	s_add_i32 s8, s6, 0x606018
	s_mul_i32 s9, s5, 0x180c
	s_add_i32 s9, s9, s33
	s_add_i32 s4, s34, 3
	s_min_i32 s4, s4, 0x200
	s_mul_i32 s4, s4, 0x804
	s_add_i32 s4, s4, s38
	buffer_load_dword v24, v28, s[20:23], s4 offen nt
	buffer_load_dwordx3 v[104:106], v27, s[24:27], s9 offen nt
	buffer_load_dword v92, v28, s[16:19], s7 offen nt
	buffer_load_dword v93, v28, s[16:19], s8 offen nt
	s_waitcnt vmcnt(8)
	v_mov_b32_dpp v108, v32 wave_shr:1 row_mask:0xf bank_mask:0xf bound_ctrl:1
	v_mov_b32_dpp v109, v33 wave_shr:1 row_mask:0xf bank_mask:0xf bound_ctrl:1
	v_mov_b32_dpp v110, v34 wave_shr:1 row_mask:0xf bank_mask:0xf bound_ctrl:1
	v_mov_b32_dpp v112, v32 wave_shl:1 row_mask:0xf bank_mask:0xf bound_ctrl:1
	v_mov_b32_dpp v113, v33 wave_shl:1 row_mask:0xf bank_mask:0xf bound_ctrl:1
	v_mov_b32_dpp v114, v34 wave_shl:1 row_mask:0xf bank_mask:0xf bound_ctrl:1
	s_add_i32 s4, s34, 1
	s_cmpk_lt_u32 s4, 0x201
	s_cselect_b64 s[12:13], s[40:41], 0
	v_cmp_eq_u32_e64 s[14:15], s37, v17
	s_and_b64 s[14:15], s[14:15], s[12:13]
	v_cndmask_b32_e64 v29, 0, 1, s[14:15]
	v_pk_add_f32 v[96:97], v[32:33], v[108:109]
	v_pk_mul_f32 v[100:101], v[32:33], v[32:33] op_sel_hi:[0,1]
	v_or_b32_dpp v57, v29, v29 wave_shr:1 row_mask:0xf bank_mask:0xf bound_ctrl:1
	v_pk_mul_f32 v[116:117], v[32:33], v[34:35] op_sel_hi:[1,0]
	v_or_b32_dpp v57, v29, v57 wave_shl:1 row_mask:0xf bank_mask:0xf bound_ctrl:1
	v_mul_f32_e64 v118, v33, v33
	v_mul_f32_e64 v119, v34, v34
	v_or_b32_dpp v88, v57, v57 wave_shr:1 row_mask:0xf bank_mask:0xf bound_ctrl:1
	v_add_f32_e64 v120, v34, v110
	v_pk_add_f32 v[96:97], v[96:97], v[112:113]
	v_or_b32_dpp v88, v57, v88 wave_shl:1 row_mask:0xf bank_mask:0xf bound_ctrl:1
	v_or3_b32 v29, v88, v89, v56
	v_or3_b32 v29, v29, v37, v36
	s_add_i32 s4, s34, -2
	s_cmpk_lt_u32 s4, 0x1ff
	s_cselect_b64 s[12:13], s[42:43], 0
	v_cmp_ne_u32_e64 s[30:31], 0, v29
	s_and_b64 s[30:31], s[30:31], s[12:13]
	v_cndmask_b32_e64 v29, 0, 1.0, s[30:31]
	v_pk_fma_f32 v[100:101], v[108:109], v[108:109], v[100:101] op_sel_hi:[0,1,1]
	v_pk_fma_f32 v[116:117], v[108:109], v[110:111], v[116:117] op_sel_hi:[1,0,1]
	v_fma_f32 v118, v109, v109, v118
	v_fma_f32 v119, v110, v110, v119
	v_add_f32_dpp v121, v29, v29 wave_shr:1 row_mask:0xf bank_mask:0xf bound_ctrl:1
	v_add_f32_e64 v120, v120, v114
	v_pk_fma_f32 v[100:101], v[112:113], v[112:113], v[100:101] op_sel_hi:[0,1,1]
	v_pk_fma_f32 v[116:117], v[112:113], v[114:115], v[116:117] op_sel_hi:[1,0,1]
	v_fma_f32 v118, v113, v113, v118
	v_fma_f32 v119, v114, v114, v119
	v_add_f32_dpp v121, v29, v121 wave_shl:1 row_mask:0xf bank_mask:0xf bound_ctrl:1
	v_pk_add_f32 v[124:125], v[58:59], v[96:97]
	v_pk_add_f32 v[122:123], v[38:39], v[124:125]
	v_pk_add_f32 v[38:39], v[62:63], v[100:101]
	v_pk_add_f32 v[58:59], v[48:49], v[38:39]
	v_pk_add_f32 v[48:49], v[66:67], v[116:117]
	v_pk_add_f32 v[62:63], v[50:51], v[48:49]
	v_pk_add_f32 v[50:51], v[70:71], v[118:119]
	v_pk_add_f32 v[66:67], v[52:53], v[50:51]
	v_pk_add_f32 v[52:53], v[74:75], v[120:121]
	v_pk_add_f32 v[70:71], v[54:55], v[52:53]
	v_mul_f32_e64 v128, v122, v22
	v_mul_f32_e64 v129, v123, v22
	v_mul_f32_e64 v130, v70, v22
	v_fma_f32 v29, v58, v22, v26
	v_mul_f32_e64 v57, v59, v22
	v_mul_f32_e64 v54, v62, v22
	v_fma_f32 v55, v66, v22, v26
	v_mul_f32_e64 v74, v63, v22
	v_fma_f32 v75, v67, v22, v26
	v_fma_f32 v29, -v128, v128, v29
	v_fma_f32 v57, -v128, v129, v57
	v_fma_f32 v54, -v128, v130, v54
	v_fma_f32 v55, -v129, v129, v55
	v_fma_f32 v74, -v129, v130, v74
	v_fma_f32 v75, -v130, v130, v75
	v_mul_f32_e64 v126, v74, v74
	v_mul_f32_e64 v127, v57, v75
	v_mul_f32_e64 v140, v54, v55
	v_mul_f32_e64 v141, v54, v54
	v_mul_f32_e64 v142, v29, v74
	v_mul_f32_e64 v143, v57, v57
	v_fma_f32 v126, v55, v75, -v126
	v_fma_f32 v127, v54, v74, -v127
	v_fma_f32 v140, v57, v74, -v140
	v_fma_f32 v141, v29, v75, -v141
	v_fma_f32 v142, v57, v54, -v142
	v_fma_f32 v143, v29, v55, -v143
	v_mul_f32_e64 v144, v29, v126
	v_fma_f32 v144, v57, v127, v144
	v_fma_f32 v144, v54, v140, v144
	v_rcp_f32_e32 v144, v144
	v_cmp_ne_u32_e64 vcc, s37, v2
	v_mul_f32_e64 v144, v144, v22
	v_cndmask_b32_e64 v144, 0, v144, s[30:31]
	v_cndmask_b32_e64 v29, 0, v18, vcc
	v_cndmask_b32_e64 v137, 0, v22, s[30:31]
	v_mul_f32_e64 v131, v126, v144
	v_mul_f32_e64 v132, v127, v144
	v_mul_f32_e64 v133, v140, v144
	v_mul_f32_e64 v134, v141, v144
	v_mul_f32_e64 v135, v142, v144
	v_mul_f32_e64 v136, v143, v144
	v_add_f32_e64 v138, v71, v29
	v_mov_b32_e32 v139, v2
	ds_write_b128 v23, v[128:131]
	ds_write_b128 v23, v[132:135] offset:1024
	ds_write_b128 v23, v[136:139] offset:2048
	v_mov_b32_dpp v54, v20 wave_shr:1 row_mask:0xf bank_mask:0xf bound_ctrl:1
	v_mov_b32_dpp v55, v21 wave_shr:1 row_mask:0xf bank_mask:0xf bound_ctrl:1
	v_mov_b32_dpp v58, v20 wave_shl:1 row_mask:0xf bank_mask:0xf bound_ctrl:1
	v_mov_b32_dpp v59, v21 wave_shl:1 row_mask:0xf bank_mask:0xf bound_ctrl:1
	v_pk_mul_f32 v[140:141], v[20:21], v[32:33] op_sel_hi:[1,0]
	v_pk_mul_f32 v[144:145], v[20:21], v[32:33] op_sel:[0,1]
	v_pk_mul_f32 v[148:149], v[20:21], v[34:35] op_sel_hi:[1,0]
	v_pk_add_f32 v[152:153], v[20:21], v[54:55]
	v_pk_fma_f32 v[140:141], v[54:55], v[108:109], v[140:141] op_sel_hi:[1,0,1]
	v_pk_fma_f32 v[144:145], v[54:55], v[108:109], v[144:145] op_sel:[0,1,0]
	v_pk_fma_f32 v[148:149], v[54:55], v[110:111], v[148:149] op_sel_hi:[1,0,1]
	v_pk_add_f32 v[152:153], v[152:153], v[58:59]
	v_pk_fma_f32 v[140:141], v[58:59], v[112:113], v[140:141] op_sel_hi:[1,0,1]
	v_pk_fma_f32 v[144:145], v[58:59], v[112:113], v[144:145] op_sel:[0,1,0]
	v_pk_fma_f32 v[148:149], v[58:59], v[114:115], v[148:149] op_sel_hi:[1,0,1]
	s_waitcnt lgkmcnt(0)
	s_barrier
	s_add_i32 s5, s34, 3
	s_min_i32 s5, s5, 0x200
	s_mul_i32 s6, s5, 0x804
	s_add_i32 s6, s6, s35
	s_add_i32 s7, s6, 0x505014
	s_add_i32 s8, s6, 0x606018
	s_mul_i32 s9, s5, 0x180c
	s_add_i32 s9, s9, s33
	s_add_i32 s4, s34, 4
	s_min_i32 s4, s4, 0x200
	s_mul_i32 s4, s4, 0x804
	s_add_i32 s4, s4, s38
	buffer_load_dword v2, v28, s[20:23], s4 offen nt
	buffer_load_dwordx3 v[156:158], v27, s[24:27], s9 offen nt
	buffer_load_dword v54, v28, s[16:19], s7 offen nt
	buffer_load_dword v55, v28, s[16:19], s8 offen nt
	v_pk_add_f32 v[58:59], v[102:103], v[152:153]
	v_pk_add_f32 v[62:63], v[72:73], v[58:59]
	v_pk_add_f32 v[66:67], v[90:91], v[140:141]
	v_pk_add_f32 v[72:73], v[60:61], v[66:67]
	v_pk_add_f32 v[70:71], v[94:95], v[144:145]
	v_pk_add_f32 v[60:61], v[64:65], v[70:71]
	v_pk_add_f32 v[74:75], v[98:99], v[148:149]
	v_pk_add_f32 v[64:65], v[68:69], v[74:75]
	v_pk_fma_f32 v[72:73], v[128:129], v[62:63], v[72:73] op_sel_hi:[0,1,1] neg_lo:[1,0,0] neg_hi:[1,0,0]
	v_pk_fma_f32 v[60:61], v[128:129], v[62:63], v[60:61] op_sel:[1,0,0] neg_lo:[1,0,0] neg_hi:[1,0,0]
	v_pk_fma_f32 v[64:65], v[130:131], v[62:63], v[64:65] op_sel_hi:[0,1,1] neg_lo:[1,0,0] neg_hi:[1,0,0]
	v_pk_mul_f32 v[90:91], v[130:131], v[72:73] op_sel:[1,0]
	v_pk_mul_f32 v[94:95], v[132:133], v[72:73] op_sel_hi:[0,1]
	v_pk_mul_f32 v[98:99], v[132:133], v[72:73] op_sel:[1,0]
	v_pk_fma_f32 v[90:91], v[132:133], v[60:61], v[90:91] op_sel_hi:[0,1,1]
	v_pk_fma_f32 v[94:95], v[134:135], v[60:61], v[94:95] op_sel_hi:[0,1,1]
	v_pk_fma_f32 v[98:99], v[134:135], v[60:61], v[98:99] op_sel:[1,0,0]
	v_pk_fma_f32 v[90:91], v[132:133], v[64:65], v[90:91] op_sel:[1,0,0]
	v_pk_fma_f32 v[94:95], v[134:135], v[64:65], v[94:95] op_sel:[1,0,0]
	v_pk_fma_f32 v[98:99], v[136:137], v[64:65], v[98:99] op_sel_hi:[0,1,1]
	v_pk_mul_f32 v[68:69], v[128:129], v[90:91] op_sel_hi:[0,1]
	v_pk_fma_f32 v[68:69], v[128:129], v[94:95], v[68:69] op_sel:[1,0,0]
	v_pk_fma_f32 v[68:69], v[130:131], v[98:99], v[68:69] op_sel_hi:[0,1,1]
	v_pk_fma_f32 v[68:69], v[136:137], v[62:63], v[68:69] op_sel:[1,0,0] neg_lo:[0,0,1] neg_hi:[0,0,1]
	s_waitcnt vmcnt(8)
	v_mov_b32_dpp v8, v76 wave_shr:1 row_mask:0xf bank_mask:0xf bound_ctrl:1
	v_mov_b32_dpp v9, v77 wave_shr:1 row_mask:0xf bank_mask:0xf bound_ctrl:1
	v_mov_b32_dpp v10, v78 wave_shr:1 row_mask:0xf bank_mask:0xf bound_ctrl:1
	v_mov_b32_dpp v40, v76 wave_shl:1 row_mask:0xf bank_mask:0xf bound_ctrl:1
	v_mov_b32_dpp v41, v77 wave_shl:1 row_mask:0xf bank_mask:0xf bound_ctrl:1
	v_mov_b32_dpp v42, v78 wave_shl:1 row_mask:0xf bank_mask:0xf bound_ctrl:1
	s_add_i32 s4, s34, 2
	s_cmpk_lt_u32 s4, 0x201
	s_cselect_b64 s[12:13], s[40:41], 0
	v_cmp_eq_u32_e64 s[14:15], s37, v25
	s_and_b64 s[14:15], s[14:15], s[12:13]
	v_cndmask_b32_e64 v29, 0, 1, s[14:15]
	v_pk_add_f32 v[4:5], v[76:77], v[8:9]
	v_pk_mul_f32 v[44:45], v[76:77], v[76:77] op_sel_hi:[0,1]
	v_or_b32_dpp v36, v29, v29 wave_shr:1 row_mask:0xf bank_mask:0xf bound_ctrl:1
	v_pk_mul_f32 v[46:47], v[76:77], v[78:79] op_sel_hi:[1,0]
	v_or_b32_dpp v36, v29, v36 wave_shl:1 row_mask:0xf bank_mask:0xf bound_ctrl:1
	v_mul_f32_e64 v60, v77, v77
	v_mul_f32_e64 v61, v78, v78
	v_or_b32_dpp v57, v36, v36 wave_shr:1 row_mask:0xf bank_mask:0xf bound_ctrl:1
	v_add_f32_e64 v62, v78, v10
	v_pk_add_f32 v[4:5], v[4:5], v[40:41]
	v_or_b32_dpp v57, v36, v57 wave_shl:1 row_mask:0xf bank_mask:0xf bound_ctrl:1
	v_or3_b32 v29, v57, v88, v89
	v_or3_b32 v29, v29, v56, v37
	s_add_i32 s4, s34, -1
	s_cmpk_lt_u32 s4, 0x1ff
	s_cselect_b64 s[12:13], s[42:43], 0
	v_cmp_ne_u32_e64 s[30:31], 0, v29
	s_and_b64 s[30:31], s[30:31], s[12:13]
	v_cndmask_b32_e64 v29, 0, 1.0, s[30:31]
	v_pk_fma_f32 v[44:45], v[8:9], v[8:9], v[44:45] op_sel_hi:[0,1,1]
	v_pk_fma_f32 v[46:47], v[8:9], v[10:11], v[46:47] op_sel_hi:[1,0,1]
	v_fma_f32 v60, v9, v9, v60
	v_fma_f32 v61, v10, v10, v61
	v_add_f32_dpp v63, v29, v29 wave_shr:1 row_mask:0xf bank_mask:0xf bound_ctrl:1
	v_add_f32_e64 v62, v62, v42
	v_pk_fma_f32 v[44:45], v[40:41], v[40:41], v[44:45] op_sel_hi:[0,1,1]
	v_pk_fma_f32 v[46:47], v[40:41], v[42:43], v[46:47] op_sel_hi:[1,0,1]
	v_fma_f32 v60, v41, v41, v60
	v_fma_f32 v61, v42, v42, v61
	v_add_f32_dpp v63, v29, v63 wave_shl:1 row_mask:0xf bank_mask:0xf bound_ctrl:1
	v_pk_add_f32 v[64:65], v[124:125], v[4:5]
	v_pk_add_f32 v[72:73], v[38:39], v[44:45]
	v_pk_add_f32 v[38:39], v[48:49], v[46:47]
	v_pk_add_f32 v[48:49], v[50:51], v[60:61]
	v_pk_add_f32 v[50:51], v[52:53], v[62:63]
	v_mul_f32_e64 v124, v64, v22
	v_mul_f32_e64 v125, v65, v22
	v_mul_f32_e64 v126, v50, v22
	v_fma_f32 v29, v72, v22, v26
	v_mul_f32_e64 v36, v73, v22
	v_mul_f32_e64 v52, v38, v22
	v_fma_f32 v53, v48, v22, v26
	v_mul_f32_e64 v102, v39, v22
	v_fma_f32 v103, v49, v22, v26
	v_fma_f32 v29, -v124, v124, v29
	v_fma_f32 v36, -v124, v125, v36
	v_fma_f32 v52, -v124, v126, v52
	v_fma_f32 v53, -v125, v125, v53
	v_fma_f32 v102, -v125, v126, v102
	v_fma_f32 v103, -v126, v126, v103
	v_mul_f32_e64 v122, v102, v102
	v_mul_f32_e64 v123, v36, v103
	v_mul_f32_e64 v136, v52, v53
	v_mul_f32_e64 v137, v52, v52
	v_mul_f32_e64 v138, v29, v102
	v_mul_f32_e64 v139, v36, v36
	v_fma_f32 v122, v53, v103, -v122
	v_fma_f32 v123, v52, v102, -v123
	v_fma_f32 v136, v36, v102, -v136
	v_fma_f32 v137, v29, v103, -v137
	v_fma_f32 v138, v36, v52, -v138
	v_fma_f32 v139, v29, v53, -v139
	v_mul_f32_e64 v142, v29, v122
	v_fma_f32 v142, v36, v123, v142
	v_fma_f32 v142, v52, v136, v142
	v_rcp_f32_e32 v142, v142
	v_cmp_ne_u32_e64 vcc, s37, v3
	v_mul_f32_e64 v142, v142, v22
	v_cndmask_b32_e64 v142, 0, v142, s[30:31]
	v_cndmask_b32_e64 v29, 0, v18, vcc
	v_cndmask_b32_e64 v133, 0, v22, s[30:31]
	v_mul_f32_e64 v127, v122, v142
	v_mul_f32_e64 v128, v123, v142
	v_mul_f32_e64 v129, v136, v142
	v_mul_f32_e64 v130, v137, v142
	v_mul_f32_e64 v131, v138, v142
	v_mul_f32_e64 v132, v139, v142
	v_add_f32_e64 v134, v51, v29
	v_mov_b32_e32 v135, v3
	ds_write_b128 v23, v[124:127] offset:3072
	ds_write_b128 v23, v[128:131] offset:4096
	ds_write_b128 v23, v[132:135] offset:5120
	v_mov_b32_dpp v36, v30 wave_shr:1 row_mask:0xf bank_mask:0xf bound_ctrl:1
	v_mov_b32_dpp v37, v31 wave_shr:1 row_mask:0xf bank_mask:0xf bound_ctrl:1
	v_mov_b32_dpp v48, v30 wave_shl:1 row_mask:0xf bank_mask:0xf bound_ctrl:1
	v_mov_b32_dpp v49, v31 wave_shl:1 row_mask:0xf bank_mask:0xf bound_ctrl:1
	v_pk_mul_f32 v[38:39], v[30:31], v[76:77] op_sel_hi:[1,0]
	v_pk_mul_f32 v[50:51], v[30:31], v[76:77] op_sel:[0,1]
	v_pk_mul_f32 v[102:103], v[30:31], v[78:79] op_sel_hi:[1,0]
	v_pk_add_f32 v[122:123], v[30:31], v[36:37]
	v_pk_fma_f32 v[38:39], v[36:37], v[8:9], v[38:39] op_sel_hi:[1,0,1]
	v_pk_fma_f32 v[50:51], v[36:37], v[8:9], v[50:51] op_sel:[0,1,0]
	v_pk_fma_f32 v[102:103], v[36:37], v[10:11], v[102:103] op_sel_hi:[1,0,1]
	v_pk_add_f32 v[122:123], v[122:123], v[48:49]
	v_pk_fma_f32 v[38:39], v[48:49], v[40:41], v[38:39] op_sel_hi:[1,0,1]
	v_pk_fma_f32 v[50:51], v[48:49], v[40:41], v[50:51] op_sel:[0,1,0]
	v_pk_fma_f32 v[102:103], v[48:49], v[42:43], v[102:103] op_sel_hi:[1,0,1]
	s_waitcnt lgkmcnt(0)
	s_barrier
	s_add_i32 s5, s34, 4
	s_min_i32 s5, s5, 0x200
	s_mul_i32 s6, s5, 0x804
	s_add_i32 s6, s6, s35
	s_add_i32 s7, s6, 0x505014
	s_add_i32 s8, s6, 0x606018
	s_mul_i32 s9, s5, 0x180c
	s_add_i32 s9, s9, s33
	s_add_i32 s4, s34, 5
	s_min_i32 s4, s4, 0x200
	s_mul_i32 s4, s4, 0x804
	s_add_i32 s4, s4, s38
	buffer_load_dword v3, v28, s[20:23], s4 offen nt
	buffer_load_dwordx3 v[136:138], v27, s[24:27], s9 offen nt
	buffer_load_dword v36, v28, s[16:19], s7 offen nt
	buffer_load_dword v37, v28, s[16:19], s8 offen nt
	v_pk_add_f32 v[48:49], v[58:59], v[122:123]
	v_pk_add_f32 v[58:59], v[66:67], v[38:39]
	v_pk_add_f32 v[66:67], v[70:71], v[50:51]
	v_pk_add_f32 v[70:71], v[74:75], v[102:103]
	v_pk_fma_f32 v[58:59], v[124:125], v[48:49], v[58:59] op_sel_hi:[0,1,1] neg_lo:[1,0,0] neg_hi:[1,0,0]
	v_pk_fma_f32 v[66:67], v[124:125], v[48:49], v[66:67] op_sel:[1,0,0] neg_lo:[1,0,0] neg_hi:[1,0,0]
	v_pk_fma_f32 v[70:71], v[126:127], v[48:49], v[70:71] op_sel_hi:[0,1,1] neg_lo:[1,0,0] neg_hi:[1,0,0]
	v_pk_mul_f32 v[52:53], v[126:127], v[58:59] op_sel:[1,0]
	v_pk_mul_f32 v[64:65], v[128:129], v[58:59] op_sel_hi:[0,1]
	v_pk_mul_f32 v[72:73], v[128:129], v[58:59] op_sel:[1,0]
	v_pk_fma_f32 v[52:53], v[128:129], v[66:67], v[52:53] op_sel_hi:[0,1,1]
	v_pk_fma_f32 v[64:65], v[130:131], v[66:67], v[64:65] op_sel_hi:[0,1,1]
	v_pk_fma_f32 v[72:73], v[130:131], v[66:67], v[72:73] op_sel:[1,0,0]
	v_pk_fma_f32 v[52:53], v[128:129], v[70:71], v[52:53] op_sel:[1,0,0]
	v_pk_fma_f32 v[64:65], v[130:131], v[70:71], v[64:65] op_sel:[1,0,0]
	v_pk_fma_f32 v[72:73], v[132:133], v[70:71], v[72:73] op_sel_hi:[0,1,1]
	v_pk_mul_f32 v[74:75], v[124:125], v[52:53] op_sel_hi:[0,1]
	v_pk_fma_f32 v[74:75], v[124:125], v[64:65], v[74:75] op_sel:[1,0,0]
	v_pk_fma_f32 v[74:75], v[126:127], v[72:73], v[74:75] op_sel_hi:[0,1,1]
	v_pk_fma_f32 v[74:75], v[132:133], v[48:49], v[74:75] op_sel:[1,0,0] neg_lo:[0,0,1] neg_hi:[0,0,1]
	s_waitcnt vmcnt(8)
	v_mov_b32_dpp v12, v104 wave_shr:1 row_mask:0xf bank_mask:0xf bound_ctrl:1
	v_mov_b32_dpp v13, v105 wave_shr:1 row_mask:0xf bank_mask:0xf bound_ctrl:1
	v_mov_b32_dpp v14, v106 wave_shr:1 row_mask:0xf bank_mask:0xf bound_ctrl:1
	v_mov_b32_dpp v80, v104 wave_shl:1 row_mask:0xf bank_mask:0xf bound_ctrl:1
	v_mov_b32_dpp v81, v105 wave_shl:1 row_mask:0xf bank_mask:0xf bound_ctrl:1
	v_mov_b32_dpp v82, v106 wave_shl:1 row_mask:0xf bank_mask:0xf bound_ctrl:1
	s_add_i32 s4, s34, 3
	s_cmpk_lt_u32 s4, 0x201
	s_cselect_b64 s[12:13], s[40:41], 0
	v_cmp_eq_u32_e64 s[14:15], s37, v24
	s_and_b64 s[14:15], s[14:15], s[12:13]
	v_cndmask_b32_e64 v29, 0, 1, s[14:15]
	v_pk_add_f32 v[6:7], v[104:105], v[12:13]
	v_pk_mul_f32 v[48:49], v[104:105], v[104:105] op_sel_hi:[0,1]
	v_or_b32_dpp v84, v29, v29 wave_shr:1 row_mask:0xf bank_mask:0xf bound_ctrl:1
	v_pk_mul_f32 v[58:59], v[104:105], v[106:107] op_sel_hi:[1,0]
	v_or_b32_dpp v84, v29, v84 wave_shl:1 row_mask:0xf bank_mask:0xf bound_ctrl:1
	v_mul_f32_e64 v66, v105, v105
	v_mul_f32_e64 v67, v106, v106
	v_or_b32_dpp v85, v84, v84 wave_shr:1 row_mask:0xf bank_mask:0xf bound_ctrl:1
	v_add_f32_e64 v70, v106, v14
	v_pk_add_f32 v[6:7], v[6:7], v[80:81]
	v_or_b32_dpp v85, v84, v85 wave_shl:1 row_mask:0xf bank_mask:0xf bound_ctrl:1
	v_or3_b32 v29, v85, v57, v88
	v_or3_b32 v29, v29, v89, v56
	s_add_i32 s4, s34, 0
	s_cmpk_lt_u32 s4, 0x1ff
	s_cselect_b64 s[12:13], s[42:43], 0
	v_cmp_ne_u32_e64 s[30:31], 0, v29
	s_and_b64 s[30:31], s[30:31], s[12:13]
	v_cndmask_b32_e64 v29, 0, 1.0, s[30:31]
	v_pk_fma_f32 v[48:49], v[12:13], v[12:13], v[48:49] op_sel_hi:[0,1,1]
	v_pk_fma_f32 v[58:59], v[12:13], v[14:15], v[58:59] op_sel_hi:[1,0,1]
	v_fma_f32 v66, v13, v13, v66
	v_fma_f32 v67, v14, v14, v67
	v_add_f32_dpp v71, v29, v29 wave_shr:1 row_mask:0xf bank_mask:0xf bound_ctrl:1
	v_add_f32_e64 v70, v70, v82
	v_pk_fma_f32 v[48:49], v[80:81], v[80:81], v[48:49] op_sel_hi:[0,1,1]
	v_pk_fma_f32 v[58:59], v[80:81], v[82:83], v[58:59] op_sel_hi:[1,0,1]
	v_fma_f32 v66, v81, v81, v66
	v_fma_f32 v67, v82, v82, v67
	v_add_f32_dpp v71, v29, v71 wave_shl:1 row_mask:0xf bank_mask:0xf bound_ctrl:1
	v_pk_add_f32 v[86:87], v[4:5], v[6:7]
	v_pk_add_f32 v[124:125], v[96:97], v[86:87]
	v_pk_add_f32 v[126:127], v[44:45], v[48:49]
	v_pk_add_f32 v[4:5], v[100:101], v[126:127]
	v_pk_add_f32 v[130:131], v[46:47], v[58:59]
	v_pk_add_f32 v[44:45], v[116:117], v[130:131]
	v_pk_add_f32 v[96:97], v[60:61], v[66:67]
	v_pk_add_f32 v[46:47], v[118:119], v[96:97]
	v_pk_add_f32 v[118:119], v[62:63], v[70:71]
	v_pk_add_f32 v[60:61], v[120:121], v[118:119]
	v_mul_f32_e64 v132, v124, v22
	v_mul_f32_e64 v133, v125, v22
	v_mul_f32_e64 v134, v60, v22
	v_fma_f32 v29, v4, v22, v26
	v_mul_f32_e64 v84, v5, v22
	v_mul_f32_e64 v62, v44, v22
	v_fma_f32 v63, v46, v22, v26
	v_mul_f32_e64 v100, v45, v22
	v_fma_f32 v101, v47, v22, v26
	v_fma_f32 v29, -v132, v132, v29
	v_fma_f32 v84, -v132, v133, v84
	v_fma_f32 v62, -v132, v134, v62
	v_fma_f32 v63, -v133, v133, v63
	v_fma_f32 v100, -v133, v134, v100
	v_fma_f32 v101, -v134, v134, v101
	v_mul_f32_e64 v116, v100, v100
	v_mul_f32_e64 v117, v84, v101
	v_mul_f32_e64 v120, v62, v63
	v_mul_f32_e64 v121, v62, v62
	v_mul_f32_e64 v128, v29, v100
	v_mul_f32_e64 v129, v84, v84
	v_fma_f32 v116, v63, v101, -v116
	v_fma_f32 v117, v62, v100, -v117
	v_fma_f32 v120, v84, v100, -v120
	v_fma_f32 v121, v29, v101, -v121
	v_fma_f32 v128, v84, v62, -v128
	v_fma_f32 v129, v29, v63, -v129
	v_mul_f32_e64 v142, v29, v116
	v_fma_f32 v142, v84, v117, v142
	v_fma_f32 v142, v62, v120, v142
	v_rcp_f32_e32 v142, v142
	v_cmp_ne_u32_e64 vcc, s37, v16
	v_mul_f32_e64 v142, v142, v22
	v_cndmask_b32_e64 v142, 0, v142, s[30:31]
	v_cndmask_b32_e64 v29, 0, v18, vcc
	v_cndmask_b32_e64 v165, 0, v22, s[30:31]
	v_mul_f32_e64 v135, v116, v142
	v_mul_f32_e64 v160, v117, v142
	v_mul_f32_e64 v161, v120, v142
	v_mul_f32_e64 v162, v121, v142
	v_mul_f32_e64 v163, v128, v142
	v_mul_f32_e64 v164, v129, v142
	v_add_f32_e64 v166, v61, v29
	v_mov_b32_e32 v167, v16
	ds_write_b128 v23, v[132:135]
	ds_write_b128 v23, v[160:163] offset:1024
	ds_write_b128 v23, v[164:167] offset:2048
	v_mov_b32_dpp v46, v92 wave_shr:1 row_mask:0xf bank_mask:0xf bound_ctrl:1
	v_mov_b32_dpp v47, v93 wave_shr:1 row_mask:0xf bank_mask:0xf bound_ctrl:1
	v_mov_b32_dpp v62, v92 wave_shl:1 row_mask:0xf bank_mask:0xf bound_ctrl:1
	v_mov_b32_dpp v63, v93 wave_shl:1 row_mask:0xf bank_mask:0xf bound_ctrl:1
	v_pk_mul_f32 v[4:5], v[92:93], v[104:105] op_sel_hi:[1,0]
	v_pk_mul_f32 v[44:45], v[92:93], v[104:105] op_sel:[0,1]
	v_pk_mul_f32 v[60:61], v[92:93], v[106:107] op_sel_hi:[1,0]
	v_pk_add_f32 v[100:101], v[92:93], v[46:47]
	v_pk_fma_f32 v[4:5], v[46:47], v[12:13], v[4:5] op_sel_hi:[1,0,1]
	v_pk_fma_f32 v[44:45], v[46:47], v[12:13], v[44:45] op_sel:[0,1,0]
	v_pk_fma_f32 v[60:61], v[46:47], v[14:15], v[60:61] op_sel_hi:[1,0,1]
	v_pk_add_f32 v[100:101], v[100:101], v[62:63]
	v_pk_fma_f32 v[4:5], v[62:63], v[80:81], v[4:5] op_sel_hi:[1,0,1]
	v_pk_fma_f32 v[44:45], v[62:63], v[80:81], v[44:45] op_sel:[0,1,0]
	v_pk_fma_f32 v[60:61], v[62:63], v[82:83], v[60:61] op_sel_hi:[1,0,1]
	s_waitcnt lgkmcnt(0)
	s_barrier
	s_add_i32 s5, s34, 5
	s_min_i32 s5, s5, 0x200
	s_mul_i32 s6, s5, 0x804
	s_add_i32 s6, s6, s35
	s_add_i32 s7, s6, 0x505014
	s_add_i32 s8, s6, 0x606018
	s_mul_i32 s9, s5, 0x180c
	s_add_i32 s9, s9, s33
	s_add_i32 s4, s34, 6
	s_min_i32 s4, s4, 0x200
	s_mul_i32 s4, s4, 0x804
	s_add_i32 s4, s4, s38
	buffer_load_dword v16, v28, s[20:23], s4 offen nt
	buffer_load_dwordx3 v[168:170], v27, s[24:27], s9 offen nt
	buffer_load_dword v46, v28, s[16:19], s7 offen nt
	buffer_load_dword v47, v28, s[16:19], s8 offen nt
	v_pk_add_f32 v[62:63], v[122:123], v[100:101]
	v_pk_add_f32 v[116:117], v[152:153], v[62:63]
	v_pk_add_f32 v[122:123], v[38:39], v[4:5]
	v_pk_add_f32 v[142:143], v[140:141], v[122:123]
	v_pk_add_f32 v[38:39], v[50:51], v[44:45]
	v_pk_add_f32 v[146:147], v[144:145], v[38:39]
	v_pk_add_f32 v[50:51], v[102:103], v[60:61]
	v_pk_add_f32 v[150:151], v[148:149], v[50:51]
	v_pk_fma_f32 v[142:143], v[132:133], v[116:117], v[142:143] op_sel_hi:[0,1,1] neg_lo:[1,0,0] neg_hi:[1,0,0]
	v_pk_fma_f32 v[146:147], v[132:133], v[116:117], v[146:147] op_sel:[1,0,0] neg_lo:[1,0,0] neg_hi:[1,0,0]
	v_pk_fma_f32 v[150:151], v[134:135], v[116:117], v[150:151] op_sel_hi:[0,1,1] neg_lo:[1,0,0] neg_hi:[1,0,0]
	v_pk_mul_f32 v[120:121], v[134:135], v[142:143] op_sel:[1,0]
	v_pk_mul_f32 v[124:125], v[160:161], v[142:143] op_sel_hi:[0,1]
	v_pk_mul_f32 v[128:129], v[160:161], v[142:143] op_sel:[1,0]
	v_pk_fma_f32 v[120:121], v[160:161], v[146:147], v[120:121] op_sel_hi:[0,1,1]
	v_pk_fma_f32 v[124:125], v[162:163], v[146:147], v[124:125] op_sel_hi:[0,1,1]
	v_pk_fma_f32 v[128:129], v[162:163], v[146:147], v[128:129] op_sel:[1,0,0]
	v_pk_fma_f32 v[120:121], v[160:161], v[150:151], v[120:121] op_sel:[1,0,0]
	v_pk_fma_f32 v[124:125], v[162:163], v[150:151], v[124:125] op_sel:[1,0,0]
	v_pk_fma_f32 v[128:129], v[164:165], v[150:151], v[128:129] op_sel_hi:[0,1,1]
	v_pk_mul_f32 v[102:103], v[132:133], v[120:121] op_sel_hi:[0,1]
	v_pk_fma_f32 v[102:103], v[132:133], v[124:125], v[102:103] op_sel:[1,0,0]
	v_pk_fma_f32 v[102:103], v[134:135], v[128:129], v[102:103] op_sel_hi:[0,1,1]
	v_pk_fma_f32 v[102:103], v[164:165], v[116:117], v[102:103] op_sel:[1,0,0] neg_lo:[0,0,1] neg_hi:[0,0,1]
	v_cmp_eq_u32_e64 s[10:11], 6, v167
	v_cmp_eq_u32_e64 s[14:15], 7, v167
	v_pk_add_f32 v[116:117], v[52:53], v[120:121]
	v_pk_add_f32 v[140:141], v[90:91], v[116:117]
	v_pk_add_f32 v[52:53], v[64:65], v[124:125]
	v_pk_add_f32 v[90:91], v[94:95], v[52:53]
	v_pk_add_f32 v[64:65], v[72:73], v[128:129]
	v_pk_add_f32 v[94:95], v[98:99], v[64:65]
	v_pk_add_f32 v[98:99], v[74:75], v[102:103]
	v_pk_add_f32 v[72:73], v[68:69], v[98:99]
	v_pk_fma_f32 v[68:69], v[108:109], v[140:141], v[72:73] op_sel_hi:[0,1,1]
	v_pk_fma_f32 v[144:145], v[112:113], v[140:141], v[72:73] op_sel_hi:[0,1,1]
	v_pk_fma_f32 v[68:69], v[108:109], v[90:91], v[68:69] op_sel:[1,0,0]
	v_pk_fma_f32 v[144:145], v[112:113], v[90:91], v[144:145] op_sel:[1,0,0]
	v_pk_fma_f32 v[68:69], v[110:111], v[94:95], v[68:69] op_sel_hi:[0,1,1]
	v_pk_fma_f32 v[144:145], v[114:115], v[94:95], v[144:145] op_sel_hi:[0,1,1]
	v_pk_fma_f32 v[72:73], v[32:33], v[140:141], v[72:73] op_sel_hi:[0,1,1]
	v_pk_fma_f32 v[72:73], v[32:33], v[90:91], v[72:73] op_sel:[1,0,0]
	v_pk_fma_f32 v[72:73], v[34:35], v[94:95], v[72:73] op_sel_hi:[0,1,1]
	v_cndmask_b32_e64 v74, 0, v18, s[10:11]
	v_cndmask_b32_e64 v75, 0, v18, s[14:15]
	v_add_f32_dpp v72, v68, v72 wave_shl:1 row_mask:0xf bank_mask:0xf bound_ctrl:1
	v_add_f32_dpp v73, v69, v73 wave_shl:1 row_mask:0xf bank_mask:0xf bound_ctrl:1
	s_add_i32 s4, s34, 0
	s_cmpk_lt_i32 s4, 0x201
	s_cselect_b64 s[12:13], s[0:1], 0
	v_add_f32_dpp v72, v144, v72 wave_shr:1 row_mask:0xf bank_mask:0xf bound_ctrl:1
	v_add_f32_dpp v73, v145, v73 wave_shr:1 row_mask:0xf bank_mask:0xf bound_ctrl:1
	v_pk_fma_f32 v[72:73], v[20:21], v[166:167], v[72:73] op_sel_hi:[1,0,1] neg_lo:[0,0,1] neg_hi:[0,0,1]
	v_pk_add_f32 v[72:73], v[72:73], v[74:75] neg_lo:[0,1] neg_hi:[0,1]
	v_pk_mul_f32 v[142:143], v[72:73], v[72:73]
	v_add_f32_e32 v142, v142, v143
	v_cndmask_b32_e64 v143, 0, v142, s[12:13]
	v_add_f32_e32 v1, v1, v143
	s_waitcnt vmcnt(8)
	v_mov_b32_dpp v32, v156 wave_shr:1 row_mask:0xf bank_mask:0xf bound_ctrl:1
	v_mov_b32_dpp v33, v157 wave_shr:1 row_mask:0xf bank_mask:0xf bound_ctrl:1
	v_mov_b32_dpp v34, v158 wave_shr:1 row_mask:0xf bank_mask:0xf bound_ctrl:1
	v_mov_b32_dpp v72, v156 wave_shl:1 row_mask:0xf bank_mask:0xf bound_ctrl:1
	v_mov_b32_dpp v73, v157 wave_shl:1 row_mask:0xf bank_mask:0xf bound_ctrl:1
	v_mov_b32_dpp v74, v158 wave_shl:1 row_mask:0xf bank_mask:0xf bound_ctrl:1
	s_add_i32 s4, s34, 4
	s_cmpk_lt_u32 s4, 0x201
	s_cselect_b64 s[12:13], s[40:41], 0
	v_cmp_eq_u32_e64 s[14:15], s37, v2
	s_and_b64 s[14:15], s[14:15], s[12:13]
	v_cndmask_b32_e64 v29, 0, 1, s[14:15]
	v_pk_add_f32 v[20:21], v[156:157], v[32:33]
	v_pk_mul_f32 v[68:69], v[156:157], v[156:157] op_sel_hi:[0,1]
	v_or_b32_dpp v56, v29, v29 wave_shr:1 row_mask:0xf bank_mask:0xf bound_ctrl:1
	v_pk_mul_f32 v[90:91], v[156:157], v[158:159] op_sel_hi:[1,0]
	v_or_b32_dpp v56, v29, v56 wave_shl:1 row_mask:0xf bank_mask:0xf bound_ctrl:1
	v_mul_f32_e64 v94, v157, v157
	v_mul_f32_e64 v95, v158, v158
	v_or_b32_dpp v84, v56, v56 wave_shr:1 row_mask:0xf bank_mask:0xf bound_ctrl:1
	v_add_f32_e64 v108, v158, v34
	v_pk_add_f32 v[20:21], v[20:21], v[72:73]
	v_or_b32_dpp v84, v56, v84 wave_shl:1 row_mask:0xf bank_mask:0xf bound_ctrl:1
	v_or3_b32 v29, v84, v85, v57
	v_or3_b32 v29, v29, v88, v89
	s_add_i32 s4, s34, 1
	s_cmpk_lt_u32 s4, 0x1ff
	s_cselect_b64 s[12:13], s[42:43], 0
	v_cmp_ne_u32_e64 s[30:31], 0, v29
	s_and_b64 s[30:31], s[30:31], s[12:13]
	v_cndmask_b32_e64 v29, 0, 1.0, s[30:31]
	v_pk_fma_f32 v[68:69], v[32:33], v[32:33], v[68:69] op_sel_hi:[0,1,1]
	v_pk_fma_f32 v[90:91], v[32:33], v[34:35], v[90:91] op_sel_hi:[1,0,1]
	v_fma_f32 v94, v33, v33, v94
	v_fma_f32 v95, v34, v34, v95
	v_add_f32_dpp v109, v29, v29 wave_shr:1 row_mask:0xf bank_mask:0xf bound_ctrl:1
	v_add_f32_e64 v108, v108, v74
	v_pk_fma_f32 v[68:69], v[72:73], v[72:73], v[68:69] op_sel_hi:[0,1,1]
	v_pk_fma_f32 v[90:91], v[72:73], v[74:75], v[90:91] op_sel_hi:[1,0,1]
	v_fma_f32 v94, v73, v73, v94
	v_fma_f32 v95, v74, v74, v95
	v_add_f32_dpp v109, v29, v109 wave_shl:1 row_mask:0xf bank_mask:0xf bound_ctrl:1
	v_pk_add_f32 v[110:111], v[86:87], v[20:21]
	v_pk_add_f32 v[86:87], v[126:127], v[68:69]
	v_pk_add_f32 v[112:113], v[130:131], v[90:91]
	v_pk_add_f32 v[114:115], v[96:97], v[94:95]
	v_pk_add_f32 v[96:97], v[118:119], v[108:109]
	v_mul_f32_e64 v132, v110, v22
	v_mul_f32_e64 v133, v111, v22
	v_mul_f32_e64 v134, v96, v22
	v_fma_f32 v29, v86, v22, v26
	v_mul_f32_e64 v56, v87, v22
	v_mul_f32_e64 v118, v112, v22
	v_fma_f32 v119, v114, v22, v26
	v_mul_f32_e64 v126, v113, v22
	v_fma_f32 v127, v115, v22, v26
	v_fma_f32 v29, -v132, v132, v29
	v_fma_f32 v56, -v132, v133, v56
	v_fma_f32 v118, -v132, v134, v118
	v_fma_f32 v119, -v133, v133, v119
	v_fma_f32 v126, -v133, v134, v126
	v_fma_f32 v127, -v134, v134, v127
	v_mul_f32_e64 v130, v126, v126
	v_mul_f32_e64 v131, v56, v127
	v_mul_f32_e64 v148, v118, v119
	v_mul_f32_e64 v149, v118, v118
	v_mul_f32_e64 v150, v29, v126
	v_mul_f32_e64 v151, v56, v56
	v_fma_f32 v130, v119, v127, -v130
	v_fma_f32 v131, v118, v126, -v131
	v_fma_f32 v148, v56, v126, -v148
	v_fma_f32 v149, v29, v127, -v149
	v_fma_f32 v150, v56, v118, -v150
	v_fma_f32 v151, v29, v119, -v151
	v_mul_f32_e64 v152, v29, v130
	v_fma_f32 v152, v56, v131, v152
	v_fma_f32 v152, v118, v148, v152
	v_rcp_f32_e32 v152, v152
	v_cmp_ne_u32_e64 vcc, s37, v17
	v_mul_f32_e64 v152, v152, v22
	v_cndmask_b32_e64 v152, 0, v152, s[30:31]
	v_cndmask_b32_e64 v29, 0, v18, vcc
	v_cndmask_b32_e64 v145, 0, v22, s[30:31]
	v_mul_f32_e64 v135, v130, v152
	v_mul_f32_e64 v140, v131, v152
	v_mul_f32_e64 v141, v148, v152
	v_mul_f32_e64 v142, v149, v152
	v_mul_f32_e64 v143, v150, v152
	v_mul_f32_e64 v144, v151, v152
	v_add_f32_e64 v146, v97, v29
	v_mov_b32_e32 v147, v17
	ds_write_b128 v23, v[132:135] offset:3072
	ds_write_b128 v23, v[140:143] offset:4096
	ds_write_b128 v23, v[144:147] offset:5120
	v_mov_b32_dpp v96, v54 wave_shr:1 row_mask:0xf bank_mask:0xf bound_ctrl:1
	v_mov_b32_dpp v97, v55 wave_shr:1 row_mask:0xf bank_mask:0xf bound_ctrl:1
	v_mov_b32_dpp v112, v54 wave_shl:1 row_mask:0xf bank_mask:0xf bound_ctrl:1
	v_mov_b32_dpp v113, v55 wave_shl:1 row_mask:0xf bank_mask:0xf bound_ctrl:1
	v_pk_mul_f32 v[86:87], v[54:55], v[156:157] op_sel_hi:[1,0]
	v_pk_mul_f32 v[110:111], v[54:55], v[156:157] op_sel:[0,1]
	v_pk_mul_f32 v[114:115], v[54:55], v[158:159] op_sel_hi:[1,0]
	v_pk_add_f32 v[118:119], v[54:55], v[96:97]
	v_pk_fma_f32 v[86:87], v[96:97], v[32:33], v[86:87] op_sel_hi:[1,0,1]
	v_pk_fma_f32 v[110:111], v[96:97], v[32:33], v[110:111] op_sel:[0,1,0]
	v_pk_fma_f32 v[114:115], v[96:97], v[34:35], v[114:115] op_sel_hi:[1,0,1]
	v_pk_add_f32 v[118:119], v[118:119], v[112:113]
	v_pk_fma_f32 v[86:87], v[112:113], v[72:73], v[86:87] op_sel_hi:[1,0,1]
	v_pk_fma_f32 v[110:111], v[112:113], v[72:73], v[110:111] op_sel:[0,1,0]
	v_pk_fma_f32 v[114:115], v[112:113], v[74:75], v[114:115] op_sel_hi:[1,0,1]
	s_waitcnt lgkmcnt(0)
	s_barrier
	s_add_i32 s5, s34, 6
	s_min_i32 s5, s5, 0x200
	s_mul_i32 s6, s5, 0x804
	s_add_i32 s6, s6, s35
	s_add_i32 s7, s6, 0x505014
	s_add_i32 s8, s6, 0x606018
	s_mul_i32 s9, s5, 0x180c
	s_add_i32 s9, s9, s33
	s_add_i32 s4, s34, 7
	s_min_i32 s4, s4, 0x200
	s_mul_i32 s4, s4, 0x804
	s_add_i32 s4, s4, s38
	buffer_load_dword v17, v28, s[20:23], s4 offen nt
	buffer_load_dwordx3 v[148:150], v27, s[24:27], s9 offen nt
	buffer_load_dword v96, v28, s[16:19], s7 offen nt
	buffer_load_dword v97, v28, s[16:19], s8 offen nt
	v_pk_add_f32 v[112:113], v[62:63], v[118:119]
	v_pk_add_f32 v[62:63], v[122:123], v[86:87]
	v_pk_add_f32 v[122:123], v[38:39], v[110:111]
	v_pk_add_f32 v[38:39], v[50:51], v[114:115]
	v_pk_fma_f32 v[62:63], v[132:133], v[112:113], v[62:63] op_sel_hi:[0,1,1] neg_lo:[1,0,0] neg_hi:[1,0,0]
	v_pk_fma_f32 v[122:123], v[132:133], v[112:113], v[122:123] op_sel:[1,0,0] neg_lo:[1,0,0] neg_hi:[1,0,0]
	v_pk_fma_f32 v[38:39], v[134:135], v[112:113], v[38:39] op_sel_hi:[0,1,1] neg_lo:[1,0,0] neg_hi:[1,0,0]
	v_pk_mul_f32 v[152:153], v[134:135], v[62:63] op_sel:[1,0]
	v_pk_mul_f32 v[160:161], v[140:141], v[62:63] op_sel_hi:[0,1]
	v_pk_mul_f32 v[164:165], v[140:141], v[62:63] op_sel:[1,0]
	v_pk_fma_f32 v[152:153], v[140:141], v[122:123], v[152:153] op_sel_hi:[0,1,1]
	v_pk_fma_f32 v[160:161], v[142:143], v[122:123], v[160:161] op_sel_hi:[0,1,1]
	v_pk_fma_f32 v[164:165], v[142:143], v[122:123], v[164:165] op_sel:[1,0,0]
	v_pk_fma_f32 v[152:153], v[140:141], v[38:39], v[152:153] op_sel:[1,0,0]
	v_pk_fma_f32 v[160:161], v[142:143], v[38:39], v[160:161] op_sel:[1,0,0]
	v_pk_fma_f32 v[164:165], v[144:145], v[38:39], v[164:165] op_sel_hi:[0,1,1]
	v_pk_mul_f32 v[50:51], v[132:133], v[152:153] op_sel_hi:[0,1]
	v_pk_fma_f32 v[50:51], v[132:133], v[160:161], v[50:51] op_sel:[1,0,0]
	v_pk_fma_f32 v[50:51], v[134:135], v[164:165], v[50:51] op_sel_hi:[0,1,1]
	v_pk_fma_f32 v[50:51], v[144:145], v[112:113], v[50:51] op_sel:[1,0,0] neg_lo:[0,0,1] neg_hi:[0,0,1]
	v_cmp_eq_u32_e64 s[10:11], 6, v147
	v_cmp_eq_u32_e64 s[14:15], 7, v147
	v_pk_add_f32 v[38:39], v[116:117], v[152:153]
	v_pk_add_f32 v[62:63], v[52:53], v[160:161]
	v_pk_add_f32 v[52:53], v[64:65], v[164:165]
	v_pk_add_f32 v[64:65], v[98:99], v[50:51]
	v_pk_fma_f32 v[112:113], v[8:9], v[38:39], v[64:65] op_sel_hi:[0,1,1]
	v_pk_fma_f32 v[116:117], v[40:41], v[38:39], v[64:65] op_sel_hi:[0,1,1]
	v_pk_fma_f32 v[112:113], v[8:9], v[62:63], v[112:113] op_sel:[1,0,0]
	v_pk_fma_f32 v[116:117], v[40:41], v[62:63], v[116:117] op_sel:[1,0,0]
	v_pk_fma_f32 v[112:113], v[10:11], v[52:53], v[112:113] op_sel_hi:[0,1,1]
	v_pk_fma_f32 v[116:117], v[42:43], v[52:53], v[116:117] op_sel_hi:[0,1,1]
	v_pk_fma_f32 v[64:65], v[76:77], v[38:39], v[64:65] op_sel_hi:[0,1,1]
	v_pk_fma_f32 v[64:65], v[76:77], v[62:63], v[64:65] op_sel:[1,0,0]
	v_pk_fma_f32 v[64:65], v[78:79], v[52:53], v[64:65] op_sel_hi:[0,1,1]
	v_cndmask_b32_e64 v98, 0, v18, s[10:11]
	v_cndmask_b32_e64 v99, 0, v18, s[14:15]
	v_add_f32_dpp v64, v112, v64 wave_shl:1 row_mask:0xf bank_mask:0xf bound_ctrl:1
	v_add_f32_dpp v65, v113, v65 wave_shl:1 row_mask:0xf bank_mask:0xf bound_ctrl:1
	s_add_i32 s4, s34, 1
	s_cmpk_lt_i32 s4, 0x201
	s_cselect_b64 s[12:13], s[0:1], 0
	v_add_f32_dpp v64, v116, v64 wave_shr:1 row_mask:0xf bank_mask:0xf bound_ctrl:1
	v_add_f32_dpp v65, v117, v65 wave_shr:1 row_mask:0xf bank_mask:0xf bound_ctrl:1
	v_pk_fma_f32 v[64:65], v[30:31], v[146:147], v[64:65] op_sel_hi:[1,0,1] neg_lo:[0,0,1] neg_hi:[0,0,1]
	v_pk_add_f32 v[64:65], v[64:65], v[98:99] neg_lo:[0,1] neg_hi:[0,1]
	v_pk_mul_f32 v[122:123], v[64:65], v[64:65]
	v_add_f32_e32 v122, v122, v123
	v_cndmask_b32_e64 v123, 0, v122, s[12:13]
	v_add_f32_e32 v1, v1, v123
	s_waitcnt vmcnt(8)
	v_mov_b32_dpp v8, v136 wave_shr:1 row_mask:0xf bank_mask:0xf bound_ctrl:1
	v_mov_b32_dpp v9, v137 wave_shr:1 row_mask:0xf bank_mask:0xf bound_ctrl:1
	v_mov_b32_dpp v10, v138 wave_shr:1 row_mask:0xf bank_mask:0xf bound_ctrl:1
	v_mov_b32_dpp v40, v136 wave_shl:1 row_mask:0xf bank_mask:0xf bound_ctrl:1
	v_mov_b32_dpp v41, v137 wave_shl:1 row_mask:0xf bank_mask:0xf bound_ctrl:1
	v_mov_b32_dpp v42, v138 wave_shl:1 row_mask:0xf bank_mask:0xf bound_ctrl:1
	s_add_i32 s4, s34, 5
	s_cmpk_lt_u32 s4, 0x201
	s_cselect_b64 s[12:13], s[40:41], 0
	v_cmp_eq_u32_e64 s[14:15], s37, v3
	s_and_b64 s[14:15], s[14:15], s[12:13]
	v_cndmask_b32_e64 v29, 0, 1, s[14:15]
	v_pk_add_f32 v[30:31], v[136:137], v[8:9]
	v_pk_mul_f32 v[38:39], v[136:137], v[136:137] op_sel_hi:[0,1]
	v_or_b32_dpp v56, v29, v29 wave_shr:1 row_mask:0xf bank_mask:0xf bound_ctrl:1
	v_pk_mul_f32 v[52:53], v[136:137], v[138:139] op_sel_hi:[1,0]
	v_or_b32_dpp v56, v29, v56 wave_shl:1 row_mask:0xf bank_mask:0xf bound_ctrl:1
	v_mul_f32_e64 v62, v137, v137
	v_mul_f32_e64 v63, v138, v138
	v_or_b32_dpp v89, v56, v56 wave_shr:1 row_mask:0xf bank_mask:0xf bound_ctrl:1
	v_add_f32_e64 v64, v138, v10
	v_pk_add_f32 v[30:31], v[30:31], v[40:41]
	v_or_b32_dpp v89, v56, v89 wave_shl:1 row_mask:0xf bank_mask:0xf bound_ctrl:1
	v_or3_b32 v29, v89, v84, v85
	v_or3_b32 v29, v29, v57, v88
	s_add_i32 s4, s34, 2
	s_cmpk_lt_u32 s4, 0x1ff
	s_cselect_b64 s[12:13], s[42:43], 0
	v_cmp_ne_u32_e64 s[30:31], 0, v29
	s_and_b64 s[30:31], s[30:31], s[12:13]
	v_cndmask_b32_e64 v29, 0, 1.0, s[30:31]
	v_pk_fma_f32 v[38:39], v[8:9], v[8:9], v[38:39] op_sel_hi:[0,1,1]
	v_pk_fma_f32 v[52:53], v[8:9], v[10:11], v[52:53] op_sel_hi:[1,0,1]
	v_fma_f32 v62, v9, v9, v62
	v_fma_f32 v63, v10, v10, v63
	v_add_f32_dpp v65, v29, v29 wave_shr:1 row_mask:0xf bank_mask:0xf bound_ctrl:1
	v_add_f32_e64 v64, v64, v42
	v_pk_fma_f32 v[38:39], v[40:41], v[40:41], v[38:39] op_sel_hi:[0,1,1]
	v_pk_fma_f32 v[52:53], v[40:41], v[42:43], v[52:53] op_sel_hi:[1,0,1]
	v_fma_f32 v62, v41, v41, v62
	v_fma_f32 v63, v42, v42, v63
	v_add_f32_dpp v65, v29, v65 wave_shl:1 row_mask:0xf bank_mask:0xf bound_ctrl:1
	v_pk_add_f32 v[76:77], v[20:21], v[30:31]
	v_pk_add_f32 v[78:79], v[6:7], v[76:77]
	v_pk_add_f32 v[6:7], v[68:69], v[38:39]
	v_pk_add_f32 v[20:21], v[48:49], v[6:7]
	v_pk_add_f32 v[48:49], v[90:91], v[52:53]
	v_pk_add_f32 v[68:69], v[58:59], v[48:49]
	v_pk_add_f32 v[112:113], v[94:95], v[62:63]
	v_pk_add_f32 v[58:59], v[66:67], v[112:113]
	v_pk_add_f32 v[116:117], v[108:109], v[64:65]
	v_pk_add_f32 v[66:67], v[70:71], v[116:117]
	v_mul_f32_e64 v132, v78, v22
	v_mul_f32_e64 v133, v79, v22
	v_mul_f32_e64 v134, v66, v22
	v_fma_f32 v29, v20, v22, v26
	v_mul_f32_e64 v56, v21, v22
	v_mul_f32_e64 v70, v68, v22
	v_fma_f32 v71, v58, v22, v26
	v_mul_f32_e64 v90, v69, v22
	v_fma_f32 v91, v59, v22, v26
	v_fma_f32 v29, -v132, v132, v29
	v_fma_f32 v56, -v132, v133, v56
	v_fma_f32 v70, -v132, v134, v70
	v_fma_f32 v71, -v133, v133, v71
	v_fma_f32 v90, -v133, v134, v90
	v_fma_f32 v91, -v134, v134, v91
	v_mul_f32_e64 v94, v90, v90
	v_mul_f32_e64 v95, v56, v91
	v_mul_f32_e64 v98, v70, v71
	v_mul_f32_e64 v99, v70, v70
	v_mul_f32_e64 v108, v29, v90
	v_mul_f32_e64 v109, v56, v56
	v_fma_f32 v94, v71, v91, -v94
	v_fma_f32 v95, v70, v90, -v95
	v_fma_f32 v98, v56, v90, -v98
	v_fma_f32 v99, v29, v91, -v99
	v_fma_f32 v108, v56, v70, -v108
	v_fma_f32 v109, v29, v71, -v109
	v_mul_f32_e64 v122, v29, v94
	v_fma_f32 v122, v56, v95, v122
	v_fma_f32 v122, v70, v98, v122
	v_rcp_f32_e32 v122, v122
	v_cmp_ne_u32_e64 vcc, s37, v25
	v_mul_f32_e64 v122, v122, v22
	v_cndmask_b32_e64 v122, 0, v122, s[30:31]
	v_cndmask_b32_e64 v29, 0, v18, vcc
	v_cndmask_b32_e64 v145, 0, v22, s[30:31]
	v_mul_f32_e64 v135, v94, v122
	v_mul_f32_e64 v140, v95, v122
	v_mul_f32_e64 v141, v98, v122
	v_mul_f32_e64 v142, v99, v122
	v_mul_f32_e64 v143, v108, v122
	v_mul_f32_e64 v144, v109, v122
	v_add_f32_e64 v146, v67, v29
	v_mov_b32_e32 v147, v25
	ds_write_b128 v23, v[132:135]
	ds_write_b128 v23, v[140:143] offset:1024
	ds_write_b128 v23, v[144:147] offset:2048
	v_mov_b32_dpp v58, v36 wave_shr:1 row_mask:0xf bank_mask:0xf bound_ctrl:1
	v_mov_b32_dpp v59, v37 wave_shr:1 row_mask:0xf bank_mask:0xf bound_ctrl:1
	v_mov_b32_dpp v66, v36 wave_shl:1 row_mask:0xf bank_mask:0xf bound_ctrl:1
	v_mov_b32_dpp v67, v37 wave_shl:1 row_mask:0xf bank_mask:0xf bound_ctrl:1
	v_pk_mul_f32 v[20:21], v[36:37], v[136:137] op_sel_hi:[1,0]
	v_pk_mul_f32 v[68:69], v[36:37], v[136:137] op_sel:[0,1]
	v_pk_mul_f32 v[108:109], v[36:37], v[138:139] op_sel_hi:[1,0]
	v_pk_add_f32 v[172:173], v[36:37], v[58:59]
	v_pk_fma_f32 v[20:21], v[58:59], v[8:9], v[20:21] op_sel_hi:[1,0,1]
	v_pk_fma_f32 v[68:69], v[58:59], v[8:9], v[68:69] op_sel:[0,1,0]
	v_pk_fma_f32 v[108:109], v[58:59], v[10:11], v[108:109] op_sel_hi:[1,0,1]
	v_pk_add_f32 v[172:173], v[172:173], v[66:67]
	v_pk_fma_f32 v[20:21], v[66:67], v[40:41], v[20:21] op_sel_hi:[1,0,1]
	v_pk_fma_f32 v[68:69], v[66:67], v[40:41], v[68:69] op_sel:[0,1,0]
	v_pk_fma_f32 v[108:109], v[66:67], v[42:43], v[108:109] op_sel_hi:[1,0,1]
	s_waitcnt lgkmcnt(0)
	s_barrier
	s_add_i32 s5, s34, 7
	s_min_i32 s5, s5, 0x200
	s_mul_i32 s6, s5, 0x804
	s_add_i32 s6, s6, s35
	s_add_i32 s7, s6, 0x505014
	s_add_i32 s8, s6, 0x606018
	s_mul_i32 s9, s5, 0x180c
	s_add_i32 s9, s9, s33
	s_add_i32 s4, s34, 8
	s_min_i32 s4, s4, 0x200
	s_mul_i32 s4, s4, 0x804
	s_add_i32 s4, s4, s38
	buffer_load_dword v25, v28, s[20:23], s4 offen nt
	buffer_load_dwordx3 v[176:178], v27, s[24:27], s9 offen nt
	buffer_load_dword v58, v28, s[16:19], s7 offen nt
	buffer_load_dword v59, v28, s[16:19], s8 offen nt
	v_pk_add_f32 v[66:67], v[118:119], v[172:173]
	v_pk_add_f32 v[70:71], v[100:101], v[66:67]
	v_pk_add_f32 v[78:79], v[86:87], v[20:21]
	v_pk_add_f32 v[100:101], v[4:5], v[78:79]
	v_pk_add_f32 v[86:87], v[110:111], v[68:69]
	v_pk_add_f32 v[4:5], v[44:45], v[86:87]
	v_pk_add_f32 v[90:91], v[114:115], v[108:109]
	v_pk_add_f32 v[44:45], v[60:61], v[90:91]
	v_pk_fma_f32 v[100:101], v[132:133], v[70:71], v[100:101] op_sel_hi:[0,1,1] neg_lo:[1,0,0] neg_hi:[1,0,0]
	v_pk_fma_f32 v[4:5], v[132:133], v[70:71], v[4:5] op_sel:[1,0,0] neg_lo:[1,0,0] neg_hi:[1,0,0]
	v_pk_fma_f32 v[44:45], v[134:135], v[70:71], v[44:45] op_sel_hi:[0,1,1] neg_lo:[1,0,0] neg_hi:[1,0,0]
	v_pk_mul_f32 v[94:95], v[134:135], v[100:101] op_sel:[1,0]
	v_pk_mul_f32 v[98:99], v[140:141], v[100:101] op_sel_hi:[0,1]
	v_pk_mul_f32 v[110:111], v[140:141], v[100:101] op_sel:[1,0]
	v_pk_fma_f32 v[94:95], v[140:141], v[4:5], v[94:95] op_sel_hi:[0,1,1]
	v_pk_fma_f32 v[98:99], v[142:143], v[4:5], v[98:99] op_sel_hi:[0,1,1]
	v_pk_fma_f32 v[110:111], v[142:143], v[4:5], v[110:111] op_sel:[1,0,0]
	v_pk_fma_f32 v[94:95], v[140:141], v[44:45], v[94:95] op_sel:[1,0,0]
	v_pk_fma_f32 v[98:99], v[142:143], v[44:45], v[98:99] op_sel:[1,0,0]
	v_pk_fma_f32 v[110:111], v[144:145], v[44:45], v[110:111] op_sel_hi:[0,1,1]
	v_pk_mul_f32 v[60:61], v[132:133], v[94:95] op_sel_hi:[0,1]
	v_pk_fma_f32 v[60:61], v[132:133], v[98:99], v[60:61] op_sel:[1,0,0]
	v_pk_fma_f32 v[60:61], v[134:135], v[110:111], v[60:61] op_sel_hi:[0,1,1]
	v_pk_fma_f32 v[60:61], v[144:145], v[70:71], v[60:61] op_sel:[1,0,0] neg_lo:[0,0,1] neg_hi:[0,0,1]
	v_cmp_eq_u32_e64 s[10:11], 6, v147
	v_cmp_eq_u32_e64 s[14:15], 7, v147
	v_pk_add_f32 v[70:71], v[152:153], v[94:95]
	v_pk_add_f32 v[4:5], v[120:121], v[70:71]
	v_pk_add_f32 v[114:115], v[160:161], v[98:99]
	v_pk_add_f32 v[44:45], v[124:125], v[114:115]
	v_pk_add_f32 v[118:119], v[164:165], v[110:111]
	v_pk_add_f32 v[100:101], v[128:129], v[118:119]
	v_pk_add_f32 v[120:121], v[50:51], v[60:61]
	v_pk_add_f32 v[122:123], v[102:103], v[120:121]
	v_pk_fma_f32 v[50:51], v[12:13], v[4:5], v[122:123] op_sel_hi:[0,1,1]
	v_pk_fma_f32 v[102:103], v[80:81], v[4:5], v[122:123] op_sel_hi:[0,1,1]
	v_pk_fma_f32 v[50:51], v[12:13], v[44:45], v[50:51] op_sel:[1,0,0]
	v_pk_fma_f32 v[102:103], v[80:81], v[44:45], v[102:103] op_sel:[1,0,0]
	v_pk_fma_f32 v[50:51], v[14:15], v[100:101], v[50:51] op_sel_hi:[0,1,1]
	v_pk_fma_f32 v[102:103], v[82:83], v[100:101], v[102:103] op_sel_hi:[0,1,1]
	v_pk_fma_f32 v[122:123], v[104:105], v[4:5], v[122:123] op_sel_hi:[0,1,1]
	v_pk_fma_f32 v[122:123], v[104:105], v[44:45], v[122:123] op_sel:[1,0,0]
	v_pk_fma_f32 v[122:123], v[106:107], v[100:101], v[122:123] op_sel_hi:[0,1,1]
	v_cndmask_b32_e64 v124, 0, v18, s[10:11]
	v_cndmask_b32_e64 v125, 0, v18, s[14:15]
	v_add_f32_dpp v122, v50, v122 wave_shl:1 row_mask:0xf bank_mask:0xf bound_ctrl:1
	v_add_f32_dpp v123, v51, v123 wave_shl:1 row_mask:0xf bank_mask:0xf bound_ctrl:1
	s_add_i32 s4, s34, 2
	s_cmpk_lt_i32 s4, 0x201
	s_cselect_b64 s[12:13], s[0:1], 0
	v_add_f32_dpp v122, v102, v122 wave_shr:1 row_mask:0xf bank_mask:0xf bound_ctrl:1
	v_add_f32_dpp v123, v103, v123 wave_shr:1 row_mask:0xf bank_mask:0xf bound_ctrl:1
	v_pk_fma_f32 v[122:123], v[92:93], v[146:147], v[122:123] op_sel_hi:[1,0,1] neg_lo:[0,0,1] neg_hi:[0,0,1]
	v_pk_add_f32 v[122:123], v[122:123], v[124:125] neg_lo:[0,1] neg_hi:[0,1]
	v_pk_mul_f32 v[126:127], v[122:123], v[122:123]
	v_add_f32_e32 v126, v126, v127
	v_cndmask_b32_e64 v127, 0, v126, s[12:13]
	v_add_f32_e32 v1, v1, v127
	s_waitcnt vmcnt(8)
	v_mov_b32_dpp v12, v168 wave_shr:1 row_mask:0xf bank_mask:0xf bound_ctrl:1
	v_mov_b32_dpp v13, v169 wave_shr:1 row_mask:0xf bank_mask:0xf bound_ctrl:1
	v_mov_b32_dpp v14, v170 wave_shr:1 row_mask:0xf bank_mask:0xf bound_ctrl:1
	v_mov_b32_dpp v80, v168 wave_shl:1 row_mask:0xf bank_mask:0xf bound_ctrl:1
	v_mov_b32_dpp v81, v169 wave_shl:1 row_mask:0xf bank_mask:0xf bound_ctrl:1
	v_mov_b32_dpp v82, v170 wave_shl:1 row_mask:0xf bank_mask:0xf bound_ctrl:1
	s_add_i32 s4, s34, 6
	s_cmpk_lt_u32 s4, 0x201
	s_cselect_b64 s[12:13], s[40:41], 0
	v_cmp_eq_u32_e64 s[14:15], s37, v16
	s_and_b64 s[14:15], s[14:15], s[12:13]
	v_cndmask_b32_e64 v29, 0, 1, s[14:15]
	v_pk_add_f32 v[4:5], v[168:169], v[12:13]
	v_pk_mul_f32 v[44:45], v[168:169], v[168:169] op_sel_hi:[0,1]
	v_or_b32_dpp v56, v29, v29 wave_shr:1 row_mask:0xf bank_mask:0xf bound_ctrl:1
	v_pk_mul_f32 v[50:51], v[168:169], v[170:171] op_sel_hi:[1,0]
	v_or_b32_dpp v56, v29, v56 wave_shl:1 row_mask:0xf bank_mask:0xf bound_ctrl:1
	v_mul_f32_e64 v92, v169, v169
	v_mul_f32_e64 v93, v170, v170
	v_or_b32_dpp v88, v56, v56 wave_shr:1 row_mask:0xf bank_mask:0xf bound_ctrl:1
	v_add_f32_e64 v100, v170, v14
	v_pk_add_f32 v[4:5], v[4:5], v[80:81]
	v_or_b32_dpp v88, v56, v88 wave_shl:1 row_mask:0xf bank_mask:0xf bound_ctrl:1
	v_or3_b32 v29, v88, v89, v84
	v_or3_b32 v29, v29, v85, v57
	s_add_i32 s4, s34, 3
	s_cmpk_lt_u32 s4, 0x1ff
	s_cselect_b64 s[12:13], s[42:43], 0
	v_cmp_ne_u32_e64 s[30:31], 0, v29
	s_and_b64 s[30:31], s[30:31], s[12:13]
	v_cndmask_b32_e64 v29, 0, 1.0, s[30:31]
	v_pk_fma_f32 v[44:45], v[12:13], v[12:13], v[44:45] op_sel_hi:[0,1,1]
	v_pk_fma_f32 v[50:51], v[12:13], v[14:15], v[50:51] op_sel_hi:[1,0,1]
	v_fma_f32 v92, v13, v13, v92
	v_fma_f32 v93, v14, v14, v93
	v_add_f32_dpp v101, v29, v29 wave_shr:1 row_mask:0xf bank_mask:0xf bound_ctrl:1
	v_add_f32_e64 v100, v100, v82
	v_pk_fma_f32 v[44:45], v[80:81], v[80:81], v[44:45] op_sel_hi:[0,1,1]
	v_pk_fma_f32 v[50:51], v[80:81], v[82:83], v[50:51] op_sel_hi:[1,0,1]
	v_fma_f32 v92, v81, v81, v92
	v_fma_f32 v93, v82, v82, v93
	v_add_f32_dpp v101, v29, v101 wave_shl:1 row_mask:0xf bank_mask:0xf bound_ctrl:1
	v_pk_add_f32 v[102:103], v[76:77], v[4:5]
	v_pk_add_f32 v[76:77], v[6:7], v[44:45]
	v_pk_add_f32 v[6:7], v[48:49], v[50:51]
	v_pk_add_f32 v[48:49], v[112:113], v[92:93]
	v_pk_add_f32 v[104:105], v[116:117], v[100:101]
	v_mul_f32_e64 v124, v102, v22
	v_mul_f32_e64 v125, v103, v22
	v_mul_f32_e64 v126, v104, v22
	v_fma_f32 v29, v76, v22, v26
	v_mul_f32_e64 v56, v77, v22
	v_mul_f32_e64 v106, v6, v22
	v_fma_f32 v107, v48, v22, v26
	v_mul_f32_e64 v112, v7, v22
	v_fma_f32 v113, v49, v22, v26
	v_fma_f32 v29, -v124, v124, v29
	v_fma_f32 v56, -v124, v125, v56
	v_fma_f32 v106, -v124, v126, v106
	v_fma_f32 v107, -v125, v125, v107
	v_fma_f32 v112, -v125, v126, v112
	v_fma_f32 v113, -v126, v126, v113
	v_mul_f32_e64 v116, v112, v112
	v_mul_f32_e64 v117, v56, v113
	v_mul_f32_e64 v122, v106, v107
	v_mul_f32_e64 v123, v106, v106
	v_mul_f32_e64 v140, v29, v112
	v_mul_f32_e64 v141, v56, v56
	v_fma_f32 v116, v107, v113, -v116
	v_fma_f32 v117, v106, v112, -v117
	v_fma_f32 v122, v56, v112, -v122
	v_fma_f32 v123, v29, v113, -v123
	v_fma_f32 v140, v56, v106, -v140
	v_fma_f32 v141, v29, v107, -v141
	v_mul_f32_e64 v142, v29, v116
	v_fma_f32 v142, v56, v117, v142
	v_fma_f32 v142, v106, v122, v142
	v_rcp_f32_e32 v142, v142
	v_cmp_ne_u32_e64 vcc, s37, v24
	v_mul_f32_e64 v142, v142, v22
	v_cndmask_b32_e64 v142, 0, v142, s[30:31]
	v_cndmask_b32_e64 v29, 0, v18, vcc
	v_cndmask_b32_e64 v133, 0, v22, s[30:31]
	v_mul_f32_e64 v127, v116, v142
	v_mul_f32_e64 v128, v117, v142
	v_mul_f32_e64 v129, v122, v142
	v_mul_f32_e64 v130, v123, v142
	v_mul_f32_e64 v131, v140, v142
	v_mul_f32_e64 v132, v141, v142
	v_add_f32_e64 v134, v105, v29
	v_mov_b32_e32 v135, v24
	ds_write_b128 v23, v[124:127] offset:3072
	ds_write_b128 v23, v[128:131] offset:4096
	ds_write_b128 v23, v[132:135] offset:5120
	v_mov_b32_dpp v48, v46 wave_shr:1 row_mask:0xf bank_mask:0xf bound_ctrl:1
	v_mov_b32_dpp v49, v47 wave_shr:1 row_mask:0xf bank_mask:0xf bound_ctrl:1
	v_mov_b32_dpp v56, v46 wave_shl:1 row_mask:0xf bank_mask:0xf bound_ctrl:1
	v_mov_b32_dpp v57, v47 wave_shl:1 row_mask:0xf bank_mask:0xf bound_ctrl:1
	v_pk_mul_f32 v[6:7], v[46:47], v[168:169] op_sel_hi:[1,0]
	v_pk_mul_f32 v[102:103], v[46:47], v[168:169] op_sel:[0,1]
	v_pk_mul_f32 v[106:107], v[46:47], v[170:171] op_sel_hi:[1,0]
	v_pk_add_f32 v[122:123], v[46:47], v[48:49]
	v_pk_fma_f32 v[6:7], v[48:49], v[12:13], v[6:7] op_sel_hi:[1,0,1]
	v_pk_fma_f32 v[102:103], v[48:49], v[12:13], v[102:103] op_sel:[0,1,0]
	v_pk_fma_f32 v[106:107], v[48:49], v[14:15], v[106:107] op_sel_hi:[1,0,1]
	v_pk_add_f32 v[122:123], v[122:123], v[56:57]
	v_pk_fma_f32 v[6:7], v[56:57], v[80:81], v[6:7] op_sel_hi:[1,0,1]
	v_pk_fma_f32 v[102:103], v[56:57], v[80:81], v[102:103] op_sel:[0,1,0]
	v_pk_fma_f32 v[106:107], v[56:57], v[82:83], v[106:107] op_sel_hi:[1,0,1]
	s_waitcnt lgkmcnt(0)
	s_barrier
	s_add_i32 s5, s34, 8
	s_min_i32 s5, s5, 0x200
	s_mul_i32 s6, s5, 0x804
	s_add_i32 s6, s6, s35
	s_add_i32 s7, s6, 0x505014
	s_add_i32 s8, s6, 0x606018
	s_mul_i32 s9, s5, 0x180c
	s_add_i32 s9, s9, s33
	s_add_i32 s4, s34, 9
	s_min_i32 s4, s4, 0x200
	s_mul_i32 s4, s4, 0x804
	s_add_i32 s4, s4, s38
	buffer_load_dword v24, v28, s[20:23], s4 offen nt
	buffer_load_dwordx3 v[140:142], v27, s[24:27], s9 offen nt
	buffer_load_dword v48, v28, s[16:19], s7 offen nt
	buffer_load_dword v49, v28, s[16:19], s8 offen nt
	v_pk_add_f32 v[56:57], v[66:67], v[122:123]
	v_pk_add_f32 v[66:67], v[78:79], v[6:7]
	v_pk_add_f32 v[78:79], v[86:87], v[102:103]
	v_pk_add_f32 v[86:87], v[90:91], v[106:107]
	v_pk_fma_f32 v[66:67], v[124:125], v[56:57], v[66:67] op_sel_hi:[0,1,1] neg_lo:[1,0,0] neg_hi:[1,0,0]
	v_pk_fma_f32 v[78:79], v[124:125], v[56:57], v[78:79] op_sel:[1,0,0] neg_lo:[1,0,0] neg_hi:[1,0,0]
	v_pk_fma_f32 v[86:87], v[126:127], v[56:57], v[86:87] op_sel_hi:[0,1,1] neg_lo:[1,0,0] neg_hi:[1,0,0]
	v_pk_mul_f32 v[76:77], v[126:127], v[66:67] op_sel:[1,0]
	v_pk_mul_f32 v[104:105], v[128:129], v[66:67] op_sel_hi:[0,1]
	v_pk_mul_f32 v[112:113], v[128:129], v[66:67] op_sel:[1,0]
	v_pk_fma_f32 v[76:77], v[128:129], v[78:79], v[76:77] op_sel_hi:[0,1,1]
	v_pk_fma_f32 v[104:105], v[130:131], v[78:79], v[104:105] op_sel_hi:[0,1,1]
	v_pk_fma_f32 v[112:113], v[130:131], v[78:79], v[112:113] op_sel:[1,0,0]
	v_pk_fma_f32 v[76:77], v[128:129], v[86:87], v[76:77] op_sel:[1,0,0]
	v_pk_fma_f32 v[104:105], v[130:131], v[86:87], v[104:105] op_sel:[1,0,0]
	v_pk_fma_f32 v[112:113], v[132:133], v[86:87], v[112:113] op_sel_hi:[0,1,1]
	v_pk_mul_f32 v[90:91], v[124:125], v[76:77] op_sel_hi:[0,1]
	v_pk_fma_f32 v[90:91], v[124:125], v[104:105], v[90:91] op_sel:[1,0,0]
	v_pk_fma_f32 v[90:91], v[126:127], v[112:113], v[90:91] op_sel_hi:[0,1,1]
	v_pk_fma_f32 v[90:91], v[132:133], v[56:57], v[90:91] op_sel:[1,0,0] neg_lo:[0,0,1] neg_hi:[0,0,1]
	v_cmp_eq_u32_e64 s[10:11], 6, v135
	v_cmp_eq_u32_e64 s[14:15], 7, v135
	v_pk_add_f32 v[56:57], v[70:71], v[76:77]
	v_pk_add_f32 v[66:67], v[114:115], v[104:105]
	v_pk_add_f32 v[70:71], v[118:119], v[112:113]
	v_pk_add_f32 v[116:117], v[120:121], v[90:91]
	v_pk_fma_f32 v[120:121], v[32:33], v[56:57], v[116:117] op_sel_hi:[0,1,1]
	v_pk_fma_f32 v[144:145], v[72:73], v[56:57], v[116:117] op_sel_hi:[0,1,1]
	v_pk_fma_f32 v[120:121], v[32:33], v[66:67], v[120:121] op_sel:[1,0,0]
	v_pk_fma_f32 v[144:145], v[72:73], v[66:67], v[144:145] op_sel:[1,0,0]
	v_pk_fma_f32 v[120:121], v[34:35], v[70:71], v[120:121] op_sel_hi:[0,1,1]
	v_pk_fma_f32 v[144:145], v[74:75], v[70:71], v[144:145] op_sel_hi:[0,1,1]
	v_pk_fma_f32 v[116:117], v[156:157], v[56:57], v[116:117] op_sel_hi:[0,1,1]
	v_pk_fma_f32 v[116:117], v[156:157], v[66:67], v[116:117] op_sel:[1,0,0]
	v_pk_fma_f32 v[116:117], v[158:159], v[70:71], v[116:117] op_sel_hi:[0,1,1]
	v_cndmask_b32_e64 v78, 0, v18, s[10:11]
	v_cndmask_b32_e64 v79, 0, v18, s[14:15]
	v_add_f32_dpp v116, v120, v116 wave_shl:1 row_mask:0xf bank_mask:0xf bound_ctrl:1
	v_add_f32_dpp v117, v121, v117 wave_shl:1 row_mask:0xf bank_mask:0xf bound_ctrl:1
	s_add_i32 s4, s34, 3
	s_cmpk_lt_i32 s4, 0x201
	s_cselect_b64 s[12:13], s[0:1], 0
	v_add_f32_dpp v116, v144, v116 wave_shr:1 row_mask:0xf bank_mask:0xf bound_ctrl:1
	v_add_f32_dpp v117, v145, v117 wave_shr:1 row_mask:0xf bank_mask:0xf bound_ctrl:1
	v_pk_fma_f32 v[116:117], v[54:55], v[134:135], v[116:117] op_sel_hi:[1,0,1] neg_lo:[0,0,1] neg_hi:[0,0,1]
	v_pk_add_f32 v[116:117], v[116:117], v[78:79] neg_lo:[0,1] neg_hi:[0,1]
	v_pk_mul_f32 v[86:87], v[116:117], v[116:117]
	v_add_f32_e32 v86, v86, v87
	v_cndmask_b32_e64 v87, 0, v86, s[12:13]
	v_add_f32_e32 v1, v1, v87
	s_waitcnt vmcnt(8)
	v_mov_b32_dpp v32, v148 wave_shr:1 row_mask:0xf bank_mask:0xf bound_ctrl:1
	v_mov_b32_dpp v33, v149 wave_shr:1 row_mask:0xf bank_mask:0xf bound_ctrl:1
	v_mov_b32_dpp v34, v150 wave_shr:1 row_mask:0xf bank_mask:0xf bound_ctrl:1
	v_mov_b32_dpp v72, v148 wave_shl:1 row_mask:0xf bank_mask:0xf bound_ctrl:1
	v_mov_b32_dpp v73, v149 wave_shl:1 row_mask:0xf bank_mask:0xf bound_ctrl:1
	v_mov_b32_dpp v74, v150 wave_shl:1 row_mask:0xf bank_mask:0xf bound_ctrl:1
	s_add_i32 s4, s34, 7
	s_cmpk_lt_u32 s4, 0x201
	s_cselect_b64 s[12:13], s[40:41], 0
	v_cmp_eq_u32_e64 s[14:15], s37, v17
	s_and_b64 s[14:15], s[14:15], s[12:13]
	v_cndmask_b32_e64 v29, 0, 1, s[14:15]
	v_pk_add_f32 v[54:55], v[148:149], v[32:33]
	v_pk_mul_f32 v[56:57], v[148:149], v[148:149] op_sel_hi:[0,1]
	v_or_b32_dpp v86, v29, v29 wave_shr:1 row_mask:0xf bank_mask:0xf bound_ctrl:1
	v_pk_mul_f32 v[66:67], v[148:149], v[150:151] op_sel_hi:[1,0]
	v_or_b32_dpp v86, v29, v86 wave_shl:1 row_mask:0xf bank_mask:0xf bound_ctrl:1
	v_mul_f32_e64 v70, v149, v149
	v_mul_f32_e64 v71, v150, v150
	v_or_b32_dpp v87, v86, v86 wave_shr:1 row_mask:0xf bank_mask:0xf bound_ctrl:1
	v_add_f32_e64 v78, v150, v34
	v_pk_add_f32 v[54:55], v[54:55], v[72:73]
	v_or_b32_dpp v87, v86, v87 wave_shl:1 row_mask:0xf bank_mask:0xf bound_ctrl:1
	v_or3_b32 v29, v87, v88, v89
	v_or3_b32 v29, v29, v84, v85
	s_add_i32 s4, s34, 4
	s_cmpk_lt_u32 s4, 0x1ff
	s_cselect_b64 s[12:13], s[42:43], 0
	v_cmp_ne_u32_e64 s[30:31], 0, v29
	s_and_b64 s[30:31], s[30:31], s[12:13]
	v_cndmask_b32_e64 v29, 0, 1.0, s[30:31]
	v_pk_fma_f32 v[56:57], v[32:33], v[32:33], v[56:57] op_sel_hi:[0,1,1]
	v_pk_fma_f32 v[66:67], v[32:33], v[34:35], v[66:67] op_sel_hi:[1,0,1]
	v_fma_f32 v70, v33, v33, v70
	v_fma_f32 v71, v34, v34, v71
	v_add_f32_dpp v79, v29, v29 wave_shr:1 row_mask:0xf bank_mask:0xf bound_ctrl:1
	v_add_f32_e64 v78, v78, v74
	v_pk_fma_f32 v[56:57], v[72:73], v[72:73], v[56:57] op_sel_hi:[0,1,1]
	v_pk_fma_f32 v[66:67], v[72:73], v[74:75], v[66:67] op_sel_hi:[1,0,1]
	v_fma_f32 v70, v73, v73, v70
	v_fma_f32 v71, v74, v74, v71
	v_add_f32_dpp v79, v29, v79 wave_shl:1 row_mask:0xf bank_mask:0xf bound_ctrl:1
	v_pk_add_f32 v[116:117], v[4:5], v[54:55]
	v_pk_add_f32 v[114:115], v[30:31], v[116:117]
	v_pk_add_f32 v[4:5], v[44:45], v[56:57]
	v_pk_add_f32 v[30:31], v[38:39], v[4:5]
	v_pk_add_f32 v[38:39], v[50:51], v[66:67]
	v_pk_add_f32 v[44:45], v[52:53], v[38:39]
	v_pk_add_f32 v[52:53], v[92:93], v[70:71]
	v_pk_add_f32 v[50:51], v[62:63], v[52:53]
	v_pk_add_f32 v[62:63], v[100:101], v[78:79]
	v_pk_add_f32 v[92:93], v[64:65], v[62:63]
	v_mul_f32_e64 v124, v114, v22
	v_mul_f32_e64 v125, v115, v22
	v_mul_f32_e64 v126, v92, v22
	v_fma_f32 v29, v30, v22, v26
	v_mul_f32_e64 v86, v31, v22
	v_mul_f32_e64 v64, v44, v22
	v_fma_f32 v65, v50, v22, v26
	v_mul_f32_e64 v100, v45, v22
	v_fma_f32 v101, v51, v22, v26
	v_fma_f32 v29, -v124, v124, v29
	v_fma_f32 v86, -v124, v125, v86
	v_fma_f32 v64, -v124, v126, v64
	v_fma_f32 v65, -v125, v125, v65
	v_fma_f32 v100, -v125, v126, v100
	v_fma_f32 v101, -v126, v126, v101
	v_mul_f32_e64 v118, v100, v100
	v_mul_f32_e64 v119, v86, v101
	v_mul_f32_e64 v120, v64, v65
	v_mul_f32_e64 v121, v64, v64
	v_mul_f32_e64 v144, v29, v100
	v_mul_f32_e64 v145, v86, v86
	v_fma_f32 v118, v65, v101, -v118
	v_fma_f32 v119, v64, v100, -v119
	v_fma_f32 v120, v86, v100, -v120
	v_fma_f32 v121, v29, v101, -v121
	v_fma_f32 v144, v86, v64, -v144
	v_fma_f32 v145, v29, v65, -v145
	v_mul_f32_e64 v146, v29, v118
	v_fma_f32 v146, v86, v119, v146
	v_fma_f32 v146, v64, v120, v146
	v_rcp_f32_e32 v146, v146
	v_cmp_ne_u32_e64 vcc, s37, v2
	v_mul_f32_e64 v146, v146, v22
	v_cndmask_b32_e64 v146, 0, v146, s[30:31]
	v_cndmask_b32_e64 v29, 0, v18, vcc
	v_cndmask_b32_e64 v133, 0, v22, s[30:31]
	v_mul_f32_e64 v127, v118, v146
	v_mul_f32_e64 v128, v119, v146
	v_mul_f32_e64 v129, v120, v146
	v_mul_f32_e64 v130, v121, v146
	v_mul_f32_e64 v131, v144, v146
	v_mul_f32_e64 v132, v145, v146
	v_add_f32_e64 v134, v93, v29
	v_mov_b32_e32 v135, v2
	ds_write_b128 v23, v[124:127]
	ds_write_b128 v23, v[128:131] offset:1024
	ds_write_b128 v23, v[132:135] offset:2048
	v_mov_b32_dpp v30, v96 wave_shr:1 row_mask:0xf bank_mask:0xf bound_ctrl:1
	v_mov_b32_dpp v31, v97 wave_shr:1 row_mask:0xf bank_mask:0xf bound_ctrl:1
	v_mov_b32_dpp v50, v96 wave_shl:1 row_mask:0xf bank_mask:0xf bound_ctrl:1
	v_mov_b32_dpp v51, v97 wave_shl:1 row_mask:0xf bank_mask:0xf bound_ctrl:1
	v_pk_mul_f32 v[44:45], v[96:97], v[148:149] op_sel_hi:[1,0]
	v_pk_mul_f32 v[64:65], v[96:97], v[148:149] op_sel:[0,1]
	v_pk_mul_f32 v[92:93], v[96:97], v[150:151] op_sel_hi:[1,0]
	v_pk_add_f32 v[100:101], v[96:97], v[30:31]
	v_pk_fma_f32 v[44:45], v[30:31], v[32:33], v[44:45] op_sel_hi:[1,0,1]
	v_pk_fma_f32 v[64:65], v[30:31], v[32:33], v[64:65] op_sel:[0,1,0]
	v_pk_fma_f32 v[92:93], v[30:31], v[34:35], v[92:93] op_sel_hi:[1,0,1]
	v_pk_add_f32 v[100:101], v[100:101], v[50:51]
	v_pk_fma_f32 v[44:45], v[50:51], v[72:73], v[44:45] op_sel_hi:[1,0,1]
	v_pk_fma_f32 v[64:65], v[50:51], v[72:73], v[64:65] op_sel:[0,1,0]
	v_pk_fma_f32 v[92:93], v[50:51], v[74:75], v[92:93] op_sel_hi:[1,0,1]
	s_waitcnt lgkmcnt(0)
	s_barrier
	s_add_i32 s5, s34, 9
	s_min_i32 s5, s5, 0x200
	s_mul_i32 s6, s5, 0x804
	s_add_i32 s6, s6, s35
	s_add_i32 s7, s6, 0x505014
	s_add_i32 s8, s6, 0x606018
	s_mul_i32 s9, s5, 0x180c
	s_add_i32 s9, s9, s33
	s_add_i32 s4, s34, 10
	s_min_i32 s4, s4, 0x200
	s_mul_i32 s4, s4, 0x804
	s_add_i32 s4, s4, s38
	buffer_load_dword v2, v28, s[20:23], s4 offen nt
	buffer_load_dwordx3 v[144:146], v27, s[24:27], s9 offen nt
	buffer_load_dword v30, v28, s[16:19], s7 offen nt
	buffer_load_dword v31, v28, s[16:19], s8 offen nt
	v_pk_add_f32 v[50:51], v[122:123], v[100:101]
	v_pk_add_f32 v[114:115], v[172:173], v[50:51]
	v_pk_add_f32 v[118:119], v[6:7], v[44:45]
	v_pk_add_f32 v[120:121], v[20:21], v[118:119]
	v_pk_add_f32 v[6:7], v[102:103], v[64:65]
	v_pk_add_f32 v[20:21], v[68:69], v[6:7]
	v_pk_add_f32 v[102:103], v[106:107], v[92:93]
	v_pk_add_f32 v[68:69], v[108:109], v[102:103]
	v_pk_fma_f32 v[120:121], v[124:125], v[114:115], v[120:121] op_sel_hi:[0,1,1] neg_lo:[1,0,0] neg_hi:[1,0,0]
	v_pk_fma_f32 v[20:21], v[124:125], v[114:115], v[20:21] op_sel:[1,0,0] neg_lo:[1,0,0] neg_hi:[1,0,0]
	v_pk_fma_f32 v[68:69], v[126:127], v[114:115], v[68:69] op_sel_hi:[0,1,1] neg_lo:[1,0,0] neg_hi:[1,0,0]
	v_pk_mul_f32 v[106:107], v[126:127], v[120:121] op_sel:[1,0]
	v_pk_mul_f32 v[122:123], v[128:129], v[120:121] op_sel_hi:[0,1]
	v_pk_mul_f32 v[154:155], v[128:129], v[120:121] op_sel:[1,0]
	v_pk_fma_f32 v[106:107], v[128:129], v[20:21], v[106:107] op_sel_hi:[0,1,1]
	v_pk_fma_f32 v[122:123], v[130:131], v[20:21], v[122:123] op_sel_hi:[0,1,1]
	v_pk_fma_f32 v[154:155], v[130:131], v[20:21], v[154:155] op_sel:[1,0,0]
	v_pk_fma_f32 v[106:107], v[128:129], v[68:69], v[106:107] op_sel:[1,0,0]
	v_pk_fma_f32 v[122:123], v[130:131], v[68:69], v[122:123] op_sel:[1,0,0]
	v_pk_fma_f32 v[154:155], v[132:133], v[68:69], v[154:155] op_sel_hi:[0,1,1]
	v_pk_mul_f32 v[108:109], v[124:125], v[106:107] op_sel_hi:[0,1]
	v_pk_fma_f32 v[108:109], v[124:125], v[122:123], v[108:109] op_sel:[1,0,0]
	v_pk_fma_f32 v[108:109], v[126:127], v[154:155], v[108:109] op_sel_hi:[0,1,1]
	v_pk_fma_f32 v[108:109], v[132:133], v[114:115], v[108:109] op_sel:[1,0,0] neg_lo:[0,0,1] neg_hi:[0,0,1]
	v_cmp_eq_u32_e64 s[10:11], 6, v135
	v_cmp_eq_u32_e64 s[14:15], 7, v135
	v_pk_add_f32 v[20:21], v[76:77], v[106:107]
	v_pk_add_f32 v[68:69], v[94:95], v[20:21]
	v_pk_add_f32 v[76:77], v[104:105], v[122:123]
	v_pk_add_f32 v[94:95], v[98:99], v[76:77]
	v_pk_add_f32 v[104:105], v[112:113], v[154:155]
	v_pk_add_f32 v[98:99], v[110:111], v[104:105]
	v_pk_add_f32 v[110:111], v[90:91], v[108:109]
	v_pk_add_f32 v[112:113], v[60:61], v[110:111]
	v_pk_fma_f32 v[60:61], v[8:9], v[68:69], v[112:113] op_sel_hi:[0,1,1]
	v_pk_fma_f32 v[120:121], v[40:41], v[68:69], v[112:113] op_sel_hi:[0,1,1]
	v_pk_fma_f32 v[60:61], v[8:9], v[94:95], v[60:61] op_sel:[1,0,0]
	v_pk_fma_f32 v[120:121], v[40:41], v[94:95], v[120:121] op_sel:[1,0,0]
	v_pk_fma_f32 v[60:61], v[10:11], v[98:99], v[60:61] op_sel_hi:[0,1,1]
	v_pk_fma_f32 v[120:121], v[42:43], v[98:99], v[120:121] op_sel_hi:[0,1,1]
	v_pk_fma_f32 v[112:113], v[136:137], v[68:69], v[112:113] op_sel_hi:[0,1,1]
	v_pk_fma_f32 v[112:113], v[136:137], v[94:95], v[112:113] op_sel:[1,0,0]
	v_pk_fma_f32 v[112:113], v[138:139], v[98:99], v[112:113] op_sel_hi:[0,1,1]
	v_cndmask_b32_e64 v90, 0, v18, s[10:11]
	v_cndmask_b32_e64 v91, 0, v18, s[14:15]
	v_add_f32_dpp v112, v60, v112 wave_shl:1 row_mask:0xf bank_mask:0xf bound_ctrl:1
	v_add_f32_dpp v113, v61, v113 wave_shl:1 row_mask:0xf bank_mask:0xf bound_ctrl:1
	s_add_i32 s4, s34, 4
	s_cmpk_lt_i32 s4, 0x201
	s_cselect_b64 s[12:13], s[0:1], 0
	v_add_f32_dpp v112, v120, v112 wave_shr:1 row_mask:0xf bank_mask:0xf bound_ctrl:1
	v_add_f32_dpp v113, v121, v113 wave_shr:1 row_mask:0xf bank_mask:0xf bound_ctrl:1
	v_pk_fma_f32 v[112:113], v[36:37], v[134:135], v[112:113] op_sel_hi:[1,0,1] neg_lo:[0,0,1] neg_hi:[0,0,1]
	v_pk_add_f32 v[112:113], v[112:113], v[90:91] neg_lo:[0,1] neg_hi:[0,1]
	v_pk_mul_f32 v[114:115], v[112:113], v[112:113]
	v_add_f32_e32 v114, v114, v115
	v_cndmask_b32_e64 v115, 0, v114, s[12:13]
	v_add_f32_e32 v1, v1, v115
	s_waitcnt vmcnt(8)
	v_mov_b32_dpp v8, v176 wave_shr:1 row_mask:0xf bank_mask:0xf bound_ctrl:1
	v_mov_b32_dpp v9, v177 wave_shr:1 row_mask:0xf bank_mask:0xf bound_ctrl:1
	v_mov_b32_dpp v10, v178 wave_shr:1 row_mask:0xf bank_mask:0xf bound_ctrl:1
	v_mov_b32_dpp v40, v176 wave_shl:1 row_mask:0xf bank_mask:0xf bound_ctrl:1
	v_mov_b32_dpp v41, v177 wave_shl:1 row_mask:0xf bank_mask:0xf bound_ctrl:1
	v_mov_b32_dpp v42, v178 wave_shl:1 row_mask:0xf bank_mask:0xf bound_ctrl:1
	s_add_i32 s4, s34, 8
	s_cmpk_lt_u32 s4, 0x201
	s_cselect_b64 s[12:13], s[40:41], 0
	v_cmp_eq_u32_e64 s[14:15], s37, v25
	s_and_b64 s[14:15], s[14:15], s[12:13]
	v_cndmask_b32_e64 v29, 0, 1, s[14:15]
	v_pk_add_f32 v[36:37], v[176:177], v[8:9]
	v_pk_mul_f32 v[60:61], v[176:177], v[176:177] op_sel_hi:[0,1]
	v_or_b32_dpp v85, v29, v29 wave_shr:1 row_mask:0xf bank_mask:0xf bound_ctrl:1
	v_pk_mul_f32 v[68:69], v[176:177], v[178:179] op_sel_hi:[1,0]
	v_or_b32_dpp v85, v29, v85 wave_shl:1 row_mask:0xf bank_mask:0xf bound_ctrl:1
	v_mul_f32_e64 v90, v177, v177
	v_mul_f32_e64 v91, v178, v178
	v_or_b32_dpp v86, v85, v85 wave_shr:1 row_mask:0xf bank_mask:0xf bound_ctrl:1
	v_add_f32_e64 v94, v178, v10
	v_pk_add_f32 v[36:37], v[36:37], v[40:41]
	v_or_b32_dpp v86, v85, v86 wave_shl:1 row_mask:0xf bank_mask:0xf bound_ctrl:1
	v_or3_b32 v29, v86, v87, v88
	v_or3_b32 v29, v29, v89, v84
	s_add_i32 s4, s34, 5
	s_cmpk_lt_u32 s4, 0x1ff
	s_cselect_b64 s[12:13], s[42:43], 0
	v_cmp_ne_u32_e64 s[30:31], 0, v29
	s_and_b64 s[30:31], s[30:31], s[12:13]
	v_cndmask_b32_e64 v29, 0, 1.0, s[30:31]
	v_pk_fma_f32 v[60:61], v[8:9], v[8:9], v[60:61] op_sel_hi:[0,1,1]
	v_pk_fma_f32 v[68:69], v[8:9], v[10:11], v[68:69] op_sel_hi:[1,0,1]
	v_fma_f32 v90, v9, v9, v90
	v_fma_f32 v91, v10, v10, v91
	v_add_f32_dpp v95, v29, v29 wave_shr:1 row_mask:0xf bank_mask:0xf bound_ctrl:1
	v_add_f32_e64 v94, v94, v42
	v_pk_fma_f32 v[60:61], v[40:41], v[40:41], v[60:61] op_sel_hi:[0,1,1]
	v_pk_fma_f32 v[68:69], v[40:41], v[42:43], v[68:69] op_sel_hi:[1,0,1]
	v_fma_f32 v90, v41, v41, v90
	v_fma_f32 v91, v42, v42, v91
	v_add_f32_dpp v95, v29, v95 wave_shl:1 row_mask:0xf bank_mask:0xf bound_ctrl:1
	v_pk_add_f32 v[98:99], v[116:117], v[36:37]
	v_pk_add_f32 v[112:113], v[4:5], v[60:61]
	v_pk_add_f32 v[4:5], v[38:39], v[68:69]
	v_pk_add_f32 v[38:39], v[52:53], v[90:91]
	v_pk_add_f32 v[52:53], v[62:63], v[94:95]
	v_mul_f32_e64 v124, v98, v22
	v_mul_f32_e64 v125, v99, v22
	v_mul_f32_e64 v126, v52, v22
	v_fma_f32 v29, v112, v22, v26
	v_mul_f32_e64 v85, v113, v22
	v_mul_f32_e64 v62, v4, v22
	v_fma_f32 v63, v38, v22, v26
	v_mul_f32_e64 v114, v5, v22
	v_fma_f32 v115, v39, v22, v26
	v_fma_f32 v29, -v124, v124, v29
	v_fma_f32 v85, -v124, v125, v85
	v_fma_f32 v62, -v124, v126, v62
	v_fma_f32 v63, -v125, v125, v63
	v_fma_f32 v114, -v125, v126, v114
	v_fma_f32 v115, -v126, v126, v115
	v_mul_f32_e64 v116, v114, v114
	v_mul_f32_e64 v117, v85, v115
	v_mul_f32_e64 v120, v62, v63
	v_mul_f32_e64 v121, v62, v62
	v_mul_f32_e64 v136, v29, v114
	v_mul_f32_e64 v137, v85, v85
	v_fma_f32 v116, v63, v115, -v116
	v_fma_f32 v117, v62, v114, -v117
	v_fma_f32 v120, v85, v114, -v120
	v_fma_f32 v121, v29, v115, -v121
	v_fma_f32 v136, v85, v62, -v136
	v_fma_f32 v137, v29, v63, -v137
	v_mul_f32_e64 v138, v29, v116
	v_fma_f32 v138, v85, v117, v138
	v_fma_f32 v138, v62, v120, v138
	v_rcp_f32_e32 v138, v138
	v_cmp_ne_u32_e64 vcc, s37, v3
	v_mul_f32_e64 v138, v138, v22
	v_cndmask_b32_e64 v138, 0, v138, s[30:31]
	v_cndmask_b32_e64 v29, 0, v18, vcc
	v_cndmask_b32_e64 v133, 0, v22, s[30:31]
	v_mul_f32_e64 v127, v116, v138
	v_mul_f32_e64 v128, v117, v138
	v_mul_f32_e64 v129, v120, v138
	v_mul_f32_e64 v130, v121, v138
	v_mul_f32_e64 v131, v136, v138
	v_mul_f32_e64 v132, v137, v138
	v_add_f32_e64 v134, v53, v29
	v_mov_b32_e32 v135, v3
	ds_write_b128 v23, v[124:127] offset:3072
	ds_write_b128 v23, v[128:131] offset:4096
	ds_write_b128 v23, v[132:135] offset:5120
	v_mov_b32_dpp v4, v58 wave_shr:1 row_mask:0xf bank_mask:0xf bound_ctrl:1
	v_mov_b32_dpp v5, v59 wave_shr:1 row_mask:0xf bank_mask:0xf bound_ctrl:1
	v_mov_b32_dpp v52, v58 wave_shl:1 row_mask:0xf bank_mask:0xf bound_ctrl:1
	v_mov_b32_dpp v53, v59 wave_shl:1 row_mask:0xf bank_mask:0xf bound_ctrl:1
	v_pk_mul_f32 v[38:39], v[58:59], v[176:177] op_sel_hi:[1,0]
	v_pk_mul_f32 v[62:63], v[58:59], v[176:177] op_sel:[0,1]
	v_pk_mul_f32 v[98:99], v[58:59], v[178:179] op_sel_hi:[1,0]
	v_pk_add_f32 v[114:115], v[58:59], v[4:5]
	v_pk_fma_f32 v[38:39], v[4:5], v[8:9], v[38:39] op_sel_hi:[1,0,1]
	v_pk_fma_f32 v[62:63], v[4:5], v[8:9], v[62:63] op_sel:[0,1,0]
	v_pk_fma_f32 v[98:99], v[4:5], v[10:11], v[98:99] op_sel_hi:[1,0,1]
	v_pk_add_f32 v[114:115], v[114:115], v[52:53]
	v_pk_fma_f32 v[38:39], v[52:53], v[40:41], v[38:39] op_sel_hi:[1,0,1]
	v_pk_fma_f32 v[62:63], v[52:53], v[40:41], v[62:63] op_sel:[0,1,0]
	v_pk_fma_f32 v[98:99], v[52:53], v[42:43], v[98:99] op_sel_hi:[1,0,1]
	s_waitcnt lgkmcnt(0)
	s_barrier
	s_add_i32 s5, s34, 10
	s_min_i32 s5, s5, 0x200
	s_mul_i32 s6, s5, 0x804
	s_add_i32 s6, s6, s35
	s_add_i32 s7, s6, 0x505014
	s_add_i32 s8, s6, 0x606018
	s_mul_i32 s9, s5, 0x180c
	s_add_i32 s9, s9, s33
	s_add_i32 s4, s34, 11
	s_min_i32 s4, s4, 0x200
	s_mul_i32 s4, s4, 0x804
	s_add_i32 s4, s4, s38
	buffer_load_dword v3, v28, s[20:23], s4 offen nt
	buffer_load_dwordx3 v[136:138], v27, s[24:27], s9 offen nt
	buffer_load_dword v4, v28, s[16:19], s7 offen nt
	buffer_load_dword v5, v28, s[16:19], s8 offen nt
	v_pk_add_f32 v[52:53], v[50:51], v[114:115]
	v_pk_add_f32 v[50:51], v[118:119], v[38:39]
	v_pk_add_f32 v[118:119], v[6:7], v[62:63]
	v_pk_add_f32 v[6:7], v[102:103], v[98:99]
	v_pk_fma_f32 v[50:51], v[124:125], v[52:53], v[50:51] op_sel_hi:[0,1,1] neg_lo:[1,0,0] neg_hi:[1,0,0]
	v_pk_fma_f32 v[118:119], v[124:125], v[52:53], v[118:119] op_sel:[1,0,0] neg_lo:[1,0,0] neg_hi:[1,0,0]
	v_pk_fma_f32 v[6:7], v[126:127], v[52:53], v[6:7] op_sel_hi:[0,1,1] neg_lo:[1,0,0] neg_hi:[1,0,0]
	v_pk_mul_f32 v[84:85], v[126:127], v[50:51] op_sel:[1,0]
	v_pk_mul_f32 v[112:113], v[128:129], v[50:51] op_sel_hi:[0,1]
	v_pk_mul_f32 v[116:117], v[128:129], v[50:51] op_sel:[1,0]
	v_pk_fma_f32 v[84:85], v[128:129], v[118:119], v[84:85] op_sel_hi:[0,1,1]
	v_pk_fma_f32 v[112:113], v[130:131], v[118:119], v[112:113] op_sel_hi:[0,1,1]
	v_pk_fma_f32 v[116:117], v[130:131], v[118:119], v[116:117] op_sel:[1,0,0]
	v_pk_fma_f32 v[84:85], v[128:129], v[6:7], v[84:85] op_sel:[1,0,0]
	v_pk_fma_f32 v[112:113], v[130:131], v[6:7], v[112:113] op_sel:[1,0,0]
	v_pk_fma_f32 v[116:117], v[132:133], v[6:7], v[116:117] op_sel_hi:[0,1,1]
	v_pk_mul_f32 v[102:103], v[124:125], v[84:85] op_sel_hi:[0,1]
	v_pk_fma_f32 v[102:103], v[124:125], v[112:113], v[102:103] op_sel:[1,0,0]
	v_pk_fma_f32 v[102:103], v[126:127], v[116:117], v[102:103] op_sel_hi:[0,1,1]
	v_pk_fma_f32 v[102:103], v[132:133], v[52:53], v[102:103] op_sel:[1,0,0] neg_lo:[0,0,1] neg_hi:[0,0,1]
	v_cmp_eq_u32_e64 s[10:11], 6, v135
	v_cmp_eq_u32_e64 s[14:15], 7, v135
	v_pk_add_f32 v[6:7], v[20:21], v[84:85]
	v_pk_add_f32 v[20:21], v[76:77], v[112:113]
	v_pk_add_f32 v[50:51], v[104:105], v[116:117]
	v_pk_add_f32 v[52:53], v[110:111], v[102:103]
	v_pk_fma_f32 v[76:77], v[12:13], v[6:7], v[52:53] op_sel_hi:[0,1,1]
	v_pk_fma_f32 v[104:105], v[80:81], v[6:7], v[52:53] op_sel_hi:[0,1,1]
	v_pk_fma_f32 v[76:77], v[12:13], v[20:21], v[76:77] op_sel:[1,0,0]
	v_pk_fma_f32 v[104:105], v[80:81], v[20:21], v[104:105] op_sel:[1,0,0]
	v_pk_fma_f32 v[76:77], v[14:15], v[50:51], v[76:77] op_sel_hi:[0,1,1]
	v_pk_fma_f32 v[104:105], v[82:83], v[50:51], v[104:105] op_sel_hi:[0,1,1]
	v_pk_fma_f32 v[52:53], v[168:169], v[6:7], v[52:53] op_sel_hi:[0,1,1]
	v_pk_fma_f32 v[52:53], v[168:169], v[20:21], v[52:53] op_sel:[1,0,0]
	v_pk_fma_f32 v[52:53], v[170:171], v[50:51], v[52:53] op_sel_hi:[0,1,1]
	v_cndmask_b32_e64 v110, 0, v18, s[10:11]
	v_cndmask_b32_e64 v111, 0, v18, s[14:15]
	v_add_f32_dpp v52, v76, v52 wave_shl:1 row_mask:0xf bank_mask:0xf bound_ctrl:1
	v_add_f32_dpp v53, v77, v53 wave_shl:1 row_mask:0xf bank_mask:0xf bound_ctrl:1
	s_add_i32 s4, s34, 5
	s_cmpk_lt_i32 s4, 0x201
	s_cselect_b64 s[12:13], s[0:1], 0
	v_add_f32_dpp v52, v104, v52 wave_shr:1 row_mask:0xf bank_mask:0xf bound_ctrl:1
	v_add_f32_dpp v53, v105, v53 wave_shr:1 row_mask:0xf bank_mask:0xf bound_ctrl:1
	v_pk_fma_f32 v[52:53], v[46:47], v[134:135], v[52:53] op_sel_hi:[1,0,1] neg_lo:[0,0,1] neg_hi:[0,0,1]
	v_pk_add_f32 v[52:53], v[52:53], v[110:111] neg_lo:[0,1] neg_hi:[0,1]
	v_pk_mul_f32 v[118:119], v[52:53], v[52:53]
	v_add_f32_e32 v118, v118, v119
	v_cndmask_b32_e64 v119, 0, v118, s[12:13]
	v_add_f32_e32 v1, v1, v119
	s_waitcnt vmcnt(8)
	v_mov_b32_dpp v12, v140 wave_shr:1 row_mask:0xf bank_mask:0xf bound_ctrl:1
	v_mov_b32_dpp v13, v141 wave_shr:1 row_mask:0xf bank_mask:0xf bound_ctrl:1
	v_mov_b32_dpp v14, v142 wave_shr:1 row_mask:0xf bank_mask:0xf bound_ctrl:1
	v_mov_b32_dpp v80, v140 wave_shl:1 row_mask:0xf bank_mask:0xf bound_ctrl:1
	v_mov_b32_dpp v81, v141 wave_shl:1 row_mask:0xf bank_mask:0xf bound_ctrl:1
	v_mov_b32_dpp v82, v142 wave_shl:1 row_mask:0xf bank_mask:0xf bound_ctrl:1
	s_add_i32 s4, s34, 9
	s_cmpk_lt_u32 s4, 0x201
	s_cselect_b64 s[12:13], s[40:41], 0
	v_cmp_eq_u32_e64 s[14:15], s37, v24
	s_and_b64 s[14:15], s[14:15], s[12:13]
	v_cndmask_b32_e64 v29, 0, 1, s[14:15]
	v_pk_add_f32 v[6:7], v[140:141], v[12:13]
	v_pk_mul_f32 v[20:21], v[140:141], v[140:141] op_sel_hi:[0,1]
	v_or_b32_dpp v76, v29, v29 wave_shr:1 row_mask:0xf bank_mask:0xf bound_ctrl:1
	v_pk_mul_f32 v[46:47], v[140:141], v[142:143] op_sel_hi:[1,0]
	v_or_b32_dpp v76, v29, v76 wave_shl:1 row_mask:0xf bank_mask:0xf bound_ctrl:1
	v_mul_f32_e64 v50, v141, v141
	v_mul_f32_e64 v51, v142, v142
	v_or_b32_dpp v77, v76, v76 wave_shr:1 row_mask:0xf bank_mask:0xf bound_ctrl:1
	v_add_f32_e64 v52, v142, v14
	v_pk_add_f32 v[6:7], v[6:7], v[80:81]
	v_or_b32_dpp v77, v76, v77 wave_shl:1 row_mask:0xf bank_mask:0xf bound_ctrl:1
	v_or3_b32 v29, v77, v86, v87
	v_or3_b32 v29, v29, v88, v89
	s_add_i32 s4, s34, 6
	s_cmpk_lt_u32 s4, 0x1ff
	s_cselect_b64 s[12:13], s[42:43], 0
	v_cmp_ne_u32_e64 s[30:31], 0, v29
	s_and_b64 s[30:31], s[30:31], s[12:13]
	v_cndmask_b32_e64 v29, 0, 1.0, s[30:31]
	v_pk_fma_f32 v[20:21], v[12:13], v[12:13], v[20:21] op_sel_hi:[0,1,1]
	v_pk_fma_f32 v[46:47], v[12:13], v[14:15], v[46:47] op_sel_hi:[1,0,1]
	v_fma_f32 v50, v13, v13, v50
	v_fma_f32 v51, v14, v14, v51
	v_add_f32_dpp v53, v29, v29 wave_shr:1 row_mask:0xf bank_mask:0xf bound_ctrl:1
	v_add_f32_e64 v52, v52, v82
	v_pk_fma_f32 v[20:21], v[80:81], v[80:81], v[20:21] op_sel_hi:[0,1,1]
	v_pk_fma_f32 v[46:47], v[80:81], v[82:83], v[46:47] op_sel_hi:[1,0,1]
	v_fma_f32 v50, v81, v81, v50
	v_fma_f32 v51, v82, v82, v51
	v_add_f32_dpp v53, v29, v53 wave_shl:1 row_mask:0xf bank_mask:0xf bound_ctrl:1
	v_pk_add_f32 v[104:105], v[36:37], v[6:7]
	v_pk_add_f32 v[110:111], v[54:55], v[104:105]
	v_pk_add_f32 v[54:55], v[60:61], v[20:21]
	v_pk_add_f32 v[36:37], v[56:57], v[54:55]
	v_pk_add_f32 v[56:57], v[68:69], v[46:47]
	v_pk_add_f32 v[60:61], v[66:67], v[56:57]
	v_pk_add_f32 v[68:69], v[90:91], v[50:51]
	v_pk_add_f32 v[66:67], v[70:71], v[68:69]
	v_pk_add_f32 v[120:121], v[94:95], v[52:53]
	v_pk_add_f32 v[70:71], v[78:79], v[120:121]
	v_mul_f32_e64 v124, v110, v22
	v_mul_f32_e64 v125, v111, v22
	v_mul_f32_e64 v126, v70, v22
	v_fma_f32 v29, v36, v22, v26
	v_mul_f32_e64 v76, v37, v22
	v_mul_f32_e64 v78, v60, v22
	v_fma_f32 v79, v66, v22, v26
	v_mul_f32_e64 v90, v61, v22
	v_fma_f32 v91, v67, v22, v26
	v_fma_f32 v29, -v124, v124, v29
	v_fma_f32 v76, -v124, v125, v76
	v_fma_f32 v78, -v124, v126, v78
	v_fma_f32 v79, -v125, v125, v79
	v_fma_f32 v90, -v125, v126, v90
	v_fma_f32 v91, -v126, v126, v91
	v_mul_f32_e64 v94, v90, v90
	v_mul_f32_e64 v95, v76, v91
	v_mul_f32_e64 v118, v78, v79
	v_mul_f32_e64 v119, v78, v78
	v_mul_f32_e64 v152, v29, v90
	v_mul_f32_e64 v153, v76, v76
	v_fma_f32 v94, v79, v91, -v94
	v_fma_f32 v95, v78, v90, -v95
	v_fma_f32 v118, v76, v90, -v118
	v_fma_f32 v119, v29, v91, -v119
	v_fma_f32 v152, v76, v78, -v152
	v_fma_f32 v153, v29, v79, -v153
	v_mul_f32_e64 v156, v29, v94
	v_fma_f32 v156, v76, v95, v156
	v_fma_f32 v156, v78, v118, v156
	v_rcp_f32_e32 v156, v156
	v_cmp_ne_u32_e64 vcc, s37, v16
	v_mul_f32_e64 v156, v156, v22
	v_cndmask_b32_e64 v156, 0, v156, s[30:31]
	v_cndmask_b32_e64 v29, 0, v18, vcc
	v_cndmask_b32_e64 v133, 0, v22, s[30:31]
	v_mul_f32_e64 v127, v94, v156
	v_mul_f32_e64 v128, v95, v156
	v_mul_f32_e64 v129, v118, v156
	v_mul_f32_e64 v130, v119, v156
	v_mul_f32_e64 v131, v152, v156
	v_mul_f32_e64 v132, v153, v156
	v_add_f32_e64 v134, v71, v29
	v_mov_b32_e32 v135, v16
	ds_write_b128 v23, v[124:127]
	ds_write_b128 v23, v[128:131] offset:1024
	ds_write_b128 v23, v[132:135] offset:2048
	v_mov_b32_dpp v66, v48 wave_shr:1 row_mask:0xf bank_mask:0xf bound_ctrl:1
	v_mov_b32_dpp v67, v49 wave_shr:1 row_mask:0xf bank_mask:0xf bound_ctrl:1
	v_mov_b32_dpp v70, v48 wave_shl:1 row_mask:0xf bank_mask:0xf bound_ctrl:1
	v_mov_b32_dpp v71, v49 wave_shl:1 row_mask:0xf bank_mask:0xf bound_ctrl:1
	v_pk_mul_f32 v[36:37], v[48:49], v[140:141] op_sel_hi:[1,0]
	v_pk_mul_f32 v[60:61], v[48:49], v[140:141] op_sel:[0,1]
	v_pk_mul_f32 v[152:153], v[48:49], v[142:143] op_sel_hi:[1,0]
	v_pk_add_f32 v[156:157], v[48:49], v[66:67]
	v_pk_fma_f32 v[36:37], v[66:67], v[12:13], v[36:37] op_sel_hi:[1,0,1]
	v_pk_fma_f32 v[60:61], v[66:67], v[12:13], v[60:61] op_sel:[0,1,0]
	v_pk_fma_f32 v[152:153], v[66:67], v[14:15], v[152:153] op_sel_hi:[1,0,1]
	v_pk_add_f32 v[156:157], v[156:157], v[70:71]
	v_pk_fma_f32 v[36:37], v[70:71], v[80:81], v[36:37] op_sel_hi:[1,0,1]
	v_pk_fma_f32 v[60:61], v[70:71], v[80:81], v[60:61] op_sel:[0,1,0]
	v_pk_fma_f32 v[152:153], v[70:71], v[82:83], v[152:153] op_sel_hi:[1,0,1]
	s_waitcnt lgkmcnt(0)
	s_barrier
	s_add_i32 s5, s34, 11
	s_min_i32 s5, s5, 0x200
	s_mul_i32 s6, s5, 0x804
	s_add_i32 s6, s6, s35
	s_add_i32 s7, s6, 0x505014
	s_add_i32 s8, s6, 0x606018
	s_mul_i32 s9, s5, 0x180c
	s_add_i32 s9, s9, s33
	s_add_i32 s4, s34, 12
	s_min_i32 s4, s4, 0x200
	s_mul_i32 s4, s4, 0x804
	s_add_i32 s4, s4, s38
	buffer_load_dword v16, v28, s[20:23], s4 offen nt
	buffer_load_dwordx3 v[160:162], v27, s[24:27], s9 offen nt
	buffer_load_dword v66, v28, s[16:19], s7 offen nt
	buffer_load_dword v67, v28, s[16:19], s8 offen nt
	v_pk_add_f32 v[70:71], v[114:115], v[156:157]
	v_pk_add_f32 v[78:79], v[100:101], v[70:71]
	v_pk_add_f32 v[90:91], v[38:39], v[36:37]
	v_pk_add_f32 v[100:101], v[44:45], v[90:91]
	v_pk_add_f32 v[38:39], v[62:63], v[60:61]
	v_pk_add_f32 v[44:45], v[64:65], v[38:39]
	v_pk_add_f32 v[62:63], v[98:99], v[152:153]
	v_pk_add_f32 v[64:65], v[92:93], v[62:63]
	v_pk_fma_f32 v[100:101], v[124:125], v[78:79], v[100:101] op_sel_hi:[0,1,1] neg_lo:[1,0,0] neg_hi:[1,0,0]
	v_pk_fma_f32 v[44:45], v[124:125], v[78:79], v[44:45] op_sel:[1,0,0] neg_lo:[1,0,0] neg_hi:[1,0,0]
	v_pk_fma_f32 v[64:65], v[126:127], v[78:79], v[64:65] op_sel_hi:[0,1,1] neg_lo:[1,0,0] neg_hi:[1,0,0]
	v_pk_mul_f32 v[94:95], v[126:127], v[100:101] op_sel:[1,0]
	v_pk_mul_f32 v[98:99], v[128:129], v[100:101] op_sel_hi:[0,1]
	v_pk_mul_f32 v[110:111], v[128:129], v[100:101] op_sel:[1,0]
	v_pk_fma_f32 v[94:95], v[128:129], v[44:45], v[94:95] op_sel_hi:[0,1,1]
	v_pk_fma_f32 v[98:99], v[130:131], v[44:45], v[98:99] op_sel_hi:[0,1,1]
	v_pk_fma_f32 v[110:111], v[130:131], v[44:45], v[110:111] op_sel:[1,0,0]
	v_pk_fma_f32 v[94:95], v[128:129], v[64:65], v[94:95] op_sel:[1,0,0]
	v_pk_fma_f32 v[98:99], v[130:131], v[64:65], v[98:99] op_sel:[1,0,0]
	v_pk_fma_f32 v[110:111], v[132:133], v[64:65], v[110:111] op_sel_hi:[0,1,1]
	v_pk_mul_f32 v[92:93], v[124:125], v[94:95] op_sel_hi:[0,1]
	v_pk_fma_f32 v[92:93], v[124:125], v[98:99], v[92:93] op_sel:[1,0,0]
	v_pk_fma_f32 v[92:93], v[126:127], v[110:111], v[92:93] op_sel_hi:[0,1,1]
	v_pk_fma_f32 v[92:93], v[132:133], v[78:79], v[92:93] op_sel:[1,0,0] neg_lo:[0,0,1] neg_hi:[0,0,1]
	v_cmp_eq_u32_e64 s[10:11], 6, v135
	v_cmp_eq_u32_e64 s[14:15], 7, v135
	v_pk_add_f32 v[44:45], v[84:85], v[94:95]
	v_pk_add_f32 v[64:65], v[106:107], v[44:45]
	v_pk_add_f32 v[84:85], v[112:113], v[98:99]
	v_pk_add_f32 v[78:79], v[122:123], v[84:85]
	v_pk_add_f32 v[100:101], v[116:117], v[110:111]
	v_pk_add_f32 v[106:107], v[154:155], v[100:101]
	v_pk_add_f32 v[114:115], v[102:103], v[92:93]
	v_pk_add_f32 v[112:113], v[108:109], v[114:115]
	v_pk_fma_f32 v[108:109], v[32:33], v[64:65], v[112:113] op_sel_hi:[0,1,1]
	v_pk_fma_f32 v[116:117], v[72:73], v[64:65], v[112:113] op_sel_hi:[0,1,1]
	v_pk_fma_f32 v[108:109], v[32:33], v[78:79], v[108:109] op_sel:[1,0,0]
	v_pk_fma_f32 v[116:117], v[72:73], v[78:79], v[116:117] op_sel:[1,0,0]
	v_pk_fma_f32 v[108:109], v[34:35], v[106:107], v[108:109] op_sel_hi:[0,1,1]
	v_pk_fma_f32 v[116:117], v[74:75], v[106:107], v[116:117] op_sel_hi:[0,1,1]
	v_pk_fma_f32 v[112:113], v[148:149], v[64:65], v[112:113] op_sel_hi:[0,1,1]
	v_pk_fma_f32 v[112:113], v[148:149], v[78:79], v[112:113] op_sel:[1,0,0]
	v_pk_fma_f32 v[112:113], v[150:151], v[106:107], v[112:113] op_sel_hi:[0,1,1]
	v_cndmask_b32_e64 v102, 0, v18, s[10:11]
	v_cndmask_b32_e64 v103, 0, v18, s[14:15]
	v_add_f32_dpp v112, v108, v112 wave_shl:1 row_mask:0xf bank_mask:0xf bound_ctrl:1
	v_add_f32_dpp v113, v109, v113 wave_shl:1 row_mask:0xf bank_mask:0xf bound_ctrl:1
	s_add_i32 s4, s34, 6
	s_cmpk_lt_i32 s4, 0x201
	s_cselect_b64 s[12:13], s[0:1], 0
	v_add_f32_dpp v112, v116, v112 wave_shr:1 row_mask:0xf bank_mask:0xf bound_ctrl:1
	v_add_f32_dpp v113, v117, v113 wave_shr:1 row_mask:0xf bank_mask:0xf bound_ctrl:1
	v_pk_fma_f32 v[112:113], v[96:97], v[134:135], v[112:113] op_sel_hi:[1,0,1] neg_lo:[0,0,1] neg_hi:[0,0,1]
	v_pk_add_f32 v[112:113], v[112:113], v[102:103] neg_lo:[0,1] neg_hi:[0,1]
	v_pk_mul_f32 v[118:119], v[112:113], v[112:113]
	v_add_f32_e32 v118, v118, v119
	v_cndmask_b32_e64 v119, 0, v118, s[12:13]
	v_add_f32_e32 v1, v1, v119
	s_waitcnt vmcnt(8)
	v_mov_b32_dpp v32, v144 wave_shr:1 row_mask:0xf bank_mask:0xf bound_ctrl:1
	v_mov_b32_dpp v33, v145 wave_shr:1 row_mask:0xf bank_mask:0xf bound_ctrl:1
	v_mov_b32_dpp v34, v146 wave_shr:1 row_mask:0xf bank_mask:0xf bound_ctrl:1
	v_mov_b32_dpp v72, v144 wave_shl:1 row_mask:0xf bank_mask:0xf bound_ctrl:1
	v_mov_b32_dpp v73, v145 wave_shl:1 row_mask:0xf bank_mask:0xf bound_ctrl:1
	v_mov_b32_dpp v74, v146 wave_shl:1 row_mask:0xf bank_mask:0xf bound_ctrl:1
	s_add_i32 s4, s34, 10
	s_cmpk_lt_u32 s4, 0x201
	s_cselect_b64 s[12:13], s[40:41], 0
	v_cmp_eq_u32_e64 s[14:15], s37, v2
	s_and_b64 s[14:15], s[14:15], s[12:13]
	v_cndmask_b32_e64 v29, 0, 1, s[14:15]
	v_pk_add_f32 v[64:65], v[144:145], v[32:33]
	v_pk_mul_f32 v[78:79], v[144:145], v[144:145] op_sel_hi:[0,1]
	v_or_b32_dpp v76, v29, v29 wave_shr:1 row_mask:0xf bank_mask:0xf bound_ctrl:1
	v_pk_mul_f32 v[96:97], v[144:145], v[146:147] op_sel_hi:[1,0]
	v_or_b32_dpp v76, v29, v76 wave_shl:1 row_mask:0xf bank_mask:0xf bound_ctrl:1
	v_mul_f32_e64 v102, v145, v145
	v_mul_f32_e64 v103, v146, v146
	v_or_b32_dpp v89, v76, v76 wave_shr:1 row_mask:0xf bank_mask:0xf bound_ctrl:1
	v_add_f32_e64 v106, v146, v34
	v_pk_add_f32 v[64:65], v[64:65], v[72:73]
	v_or_b32_dpp v89, v76, v89 wave_shl:1 row_mask:0xf bank_mask:0xf bound_ctrl:1
	v_or3_b32 v29, v89, v77, v86
	v_or3_b32 v29, v29, v87, v88
	s_add_i32 s4, s34, 7
	s_cmpk_lt_u32 s4, 0x1ff
	s_cselect_b64 s[12:13], s[42:43], 0
	v_cmp_ne_u32_e64 s[30:31], 0, v29
	s_and_b64 s[30:31], s[30:31], s[12:13]
	v_cndmask_b32_e64 v29, 0, 1.0, s[30:31]
	v_pk_fma_f32 v[78:79], v[32:33], v[32:33], v[78:79] op_sel_hi:[0,1,1]
	v_pk_fma_f32 v[96:97], v[32:33], v[34:35], v[96:97] op_sel_hi:[1,0,1]
	v_fma_f32 v102, v33, v33, v102
	v_fma_f32 v103, v34, v34, v103
	v_add_f32_dpp v107, v29, v29 wave_shr:1 row_mask:0xf bank_mask:0xf bound_ctrl:1
	v_add_f32_e64 v106, v106, v74
	v_pk_fma_f32 v[78:79], v[72:73], v[72:73], v[78:79] op_sel_hi:[0,1,1]
	v_pk_fma_f32 v[96:97], v[72:73], v[74:75], v[96:97] op_sel_hi:[1,0,1]
	v_fma_f32 v102, v73, v73, v102
	v_fma_f32 v103, v74, v74, v103
	v_add_f32_dpp v107, v29, v107 wave_shl:1 row_mask:0xf bank_mask:0xf bound_ctrl:1
	v_pk_add_f32 v[108:109], v[104:105], v[64:65]
	v_pk_add_f32 v[104:105], v[54:55], v[78:79]
	v_pk_add_f32 v[54:55], v[56:57], v[96:97]
	v_pk_add_f32 v[56:57], v[68:69], v[102:103]
	v_pk_add_f32 v[68:69], v[120:121], v[106:107]
	v_mul_f32_e64 v116, v108, v22
	v_mul_f32_e64 v117, v109, v22
	v_mul_f32_e64 v118, v68, v22
	v_fma_f32 v29, v104, v22, v26
	v_mul_f32_e64 v76, v105, v22
	v_mul_f32_e64 v112, v54, v22
	v_fma_f32 v113, v56, v22, v26
	v_mul_f32_e64 v128, v55, v22
	v_fma_f32 v129, v57, v22, v26
	v_fma_f32 v29, -v116, v116, v29
	v_fma_f32 v76, -v116, v117, v76
	v_fma_f32 v112, -v116, v118, v112
	v_fma_f32 v113, -v117, v117, v113
	v_fma_f32 v128, -v117, v118, v128
	v_fma_f32 v129, -v118, v118, v129
	v_mul_f32_e64 v130, v128, v128
	v_mul_f32_e64 v131, v76, v129
	v_mul_f32_e64 v132, v112, v113
	v_mul_f32_e64 v133, v112, v112
	v_mul_f32_e64 v134, v29, v128
	v_mul_f32_e64 v135, v76, v76
	v_fma_f32 v130, v113, v129, -v130
	v_fma_f32 v131, v112, v128, -v131
	v_fma_f32 v132, v76, v128, -v132
	v_fma_f32 v133, v29, v129, -v133
	v_fma_f32 v134, v76, v112, -v134
	v_fma_f32 v135, v29, v113, -v135
	v_mul_f32_e64 v148, v29, v130
	v_fma_f32 v148, v76, v131, v148
	v_fma_f32 v148, v112, v132, v148
	v_rcp_f32_e32 v148, v148
	v_cmp_ne_u32_e64 vcc, s37, v17
	v_mul_f32_e64 v148, v148, v22
	v_cndmask_b32_e64 v148, 0, v148, s[30:31]
	v_cndmask_b32_e64 v29, 0, v18, vcc
	v_cndmask_b32_e64 v125, 0, v22, s[30:31]
	v_mul_f32_e64 v119, v130, v148
	v_mul_f32_e64 v120, v131, v148
	v_mul_f32_e64 v121, v132, v148
	v_mul_f32_e64 v122, v133, v148
	v_mul_f32_e64 v123, v134, v148
	v_mul_f32_e64 v124, v135, v148
	v_add_f32_e64 v126, v69, v29
	v_mov_b32_e32 v127, v17
	ds_write_b128 v23, v[116:119] offset:3072
	ds_write_b128 v23, v[120:123] offset:4096
	ds_write_b128 v23, v[124:127] offset:5120
	v_mov_b32_dpp v56, v30 wave_shr:1 row_mask:0xf bank_mask:0xf bound_ctrl:1
	v_mov_b32_dpp v57, v31 wave_shr:1 row_mask:0xf bank_mask:0xf bound_ctrl:1
	v_mov_b32_dpp v68, v30 wave_shl:1 row_mask:0xf bank_mask:0xf bound_ctrl:1
	v_mov_b32_dpp v69, v31 wave_shl:1 row_mask:0xf bank_mask:0xf bound_ctrl:1
	v_pk_mul_f32 v[54:55], v[30:31], v[144:145] op_sel_hi:[1,0]
	v_pk_mul_f32 v[130:131], v[30:31], v[144:145] op_sel:[0,1]
	v_pk_mul_f32 v[134:135], v[30:31], v[146:147] op_sel_hi:[1,0]
	v_pk_add_f32 v[150:151], v[30:31], v[56:57]
	v_pk_fma_f32 v[54:55], v[56:57], v[32:33], v[54:55] op_sel_hi:[1,0,1]
	v_pk_fma_f32 v[130:131], v[56:57], v[32:33], v[130:131] op_sel:[0,1,0]
	v_pk_fma_f32 v[134:135], v[56:57], v[34:35], v[134:135] op_sel_hi:[1,0,1]
	v_pk_add_f32 v[150:151], v[150:151], v[68:69]
	v_pk_fma_f32 v[54:55], v[68:69], v[72:73], v[54:55] op_sel_hi:[1,0,1]
	v_pk_fma_f32 v[130:131], v[68:69], v[72:73], v[130:131] op_sel:[0,1,0]
	v_pk_fma_f32 v[134:135], v[68:69], v[74:75], v[134:135] op_sel_hi:[1,0,1]
	s_waitcnt lgkmcnt(0)
	s_barrier
	v_pk_add_f32 v[56:57], v[70:71], v[150:151]
	v_pk_add_f32 v[70:71], v[90:91], v[54:55]
	v_pk_add_f32 v[90:91], v[38:39], v[130:131]
	v_pk_add_f32 v[38:39], v[62:63], v[134:135]
	v_pk_fma_f32 v[70:71], v[116:117], v[56:57], v[70:71] op_sel_hi:[0,1,1] neg_lo:[1,0,0] neg_hi:[1,0,0]
	v_pk_fma_f32 v[90:91], v[116:117], v[56:57], v[90:91] op_sel:[1,0,0] neg_lo:[1,0,0] neg_hi:[1,0,0]
	v_pk_fma_f32 v[38:39], v[118:119], v[56:57], v[38:39] op_sel_hi:[0,1,1] neg_lo:[1,0,0] neg_hi:[1,0,0]
	v_pk_mul_f32 v[68:69], v[118:119], v[70:71] op_sel:[1,0]
	v_pk_mul_f32 v[104:105], v[120:121], v[70:71] op_sel_hi:[0,1]
	v_pk_mul_f32 v[108:109], v[120:121], v[70:71] op_sel:[1,0]
	v_pk_fma_f32 v[68:69], v[120:121], v[90:91], v[68:69] op_sel_hi:[0,1,1]
	v_pk_fma_f32 v[104:105], v[122:123], v[90:91], v[104:105] op_sel_hi:[0,1,1]
	v_pk_fma_f32 v[108:109], v[122:123], v[90:91], v[108:109] op_sel:[1,0,0]
	v_pk_fma_f32 v[68:69], v[120:121], v[38:39], v[68:69] op_sel:[1,0,0]
	v_pk_fma_f32 v[104:105], v[122:123], v[38:39], v[104:105] op_sel:[1,0,0]
	v_pk_fma_f32 v[108:109], v[124:125], v[38:39], v[108:109] op_sel_hi:[0,1,1]
	v_pk_mul_f32 v[62:63], v[116:117], v[68:69] op_sel_hi:[0,1]
	v_pk_fma_f32 v[62:63], v[116:117], v[104:105], v[62:63] op_sel:[1,0,0]
	v_pk_fma_f32 v[62:63], v[118:119], v[108:109], v[62:63] op_sel_hi:[0,1,1]
	v_pk_fma_f32 v[62:63], v[124:125], v[56:57], v[62:63] op_sel:[1,0,0] neg_lo:[0,0,1] neg_hi:[0,0,1]
	v_cmp_eq_u32_e64 s[10:11], 6, v127
	v_cmp_eq_u32_e64 s[14:15], 7, v127
	v_pk_add_f32 v[38:39], v[44:45], v[68:69]
	v_pk_add_f32 v[44:45], v[84:85], v[104:105]
	v_pk_add_f32 v[56:57], v[100:101], v[108:109]
	v_pk_add_f32 v[70:71], v[114:115], v[62:63]
	v_pk_fma_f32 v[90:91], v[8:9], v[38:39], v[70:71] op_sel_hi:[0,1,1]
	v_pk_fma_f32 v[114:115], v[40:41], v[38:39], v[70:71] op_sel_hi:[0,1,1]
	v_pk_fma_f32 v[90:91], v[8:9], v[44:45], v[90:91] op_sel:[1,0,0]
	v_pk_fma_f32 v[114:115], v[40:41], v[44:45], v[114:115] op_sel:[1,0,0]
	v_pk_fma_f32 v[90:91], v[10:11], v[56:57], v[90:91] op_sel_hi:[0,1,1]
	v_pk_fma_f32 v[114:115], v[42:43], v[56:57], v[114:115] op_sel_hi:[0,1,1]
	v_pk_fma_f32 v[70:71], v[176:177], v[38:39], v[70:71] op_sel_hi:[0,1,1]
	v_pk_fma_f32 v[70:71], v[176:177], v[44:45], v[70:71] op_sel:[1,0,0]
	v_pk_fma_f32 v[70:71], v[178:179], v[56:57], v[70:71] op_sel_hi:[0,1,1]
	v_cndmask_b32_e64 v84, 0, v18, s[10:11]
	v_cndmask_b32_e64 v85, 0, v18, s[14:15]
	v_add_f32_dpp v70, v90, v70 wave_shl:1 row_mask:0xf bank_mask:0xf bound_ctrl:1
	v_add_f32_dpp v71, v91, v71 wave_shl:1 row_mask:0xf bank_mask:0xf bound_ctrl:1
	s_add_i32 s4, s34, 7
	s_cmpk_lt_i32 s4, 0x201
	s_cselect_b64 s[12:13], s[0:1], 0
	v_add_f32_dpp v70, v114, v70 wave_shr:1 row_mask:0xf bank_mask:0xf bound_ctrl:1
	v_add_f32_dpp v71, v115, v71 wave_shr:1 row_mask:0xf bank_mask:0xf bound_ctrl:1
	v_pk_fma_f32 v[70:71], v[58:59], v[126:127], v[70:71] op_sel_hi:[1,0,1] neg_lo:[0,0,1] neg_hi:[0,0,1]
	v_pk_add_f32 v[70:71], v[70:71], v[84:85] neg_lo:[0,1] neg_hi:[0,1]
	v_pk_mul_f32 v[100:101], v[70:71], v[70:71]
	v_add_f32_e32 v100, v100, v101
	v_cndmask_b32_e64 v101, 0, v100, s[12:13]
	v_add_f32_e32 v1, v1, v101
	s_waitcnt vmcnt(4)
	v_mov_b32_dpp v8, v136 wave_shr:1 row_mask:0xf bank_mask:0xf bound_ctrl:1
	v_mov_b32_dpp v9, v137 wave_shr:1 row_mask:0xf bank_mask:0xf bound_ctrl:1
	v_mov_b32_dpp v10, v138 wave_shr:1 row_mask:0xf bank_mask:0xf bound_ctrl:1
	v_mov_b32_dpp v40, v136 wave_shl:1 row_mask:0xf bank_mask:0xf bound_ctrl:1
	v_mov_b32_dpp v41, v137 wave_shl:1 row_mask:0xf bank_mask:0xf bound_ctrl:1
	v_mov_b32_dpp v42, v138 wave_shl:1 row_mask:0xf bank_mask:0xf bound_ctrl:1
	s_add_i32 s4, s34, 11
	s_cmpk_lt_u32 s4, 0x201
	s_cselect_b64 s[12:13], s[40:41], 0
	v_cmp_eq_u32_e64 s[14:15], s37, v3
	s_and_b64 s[14:15], s[14:15], s[12:13]
	v_cndmask_b32_e64 v17, 0, 1, s[14:15]
	v_pk_add_f32 v[38:39], v[136:137], v[8:9]
	v_pk_mul_f32 v[44:45], v[136:137], v[136:137] op_sel_hi:[0,1]
	v_or_b32_dpp v29, v17, v17 wave_shr:1 row_mask:0xf bank_mask:0xf bound_ctrl:1
	v_pk_mul_f32 v[56:57], v[136:137], v[138:139] op_sel_hi:[1,0]
	v_or_b32_dpp v29, v17, v29 wave_shl:1 row_mask:0xf bank_mask:0xf bound_ctrl:1
	v_mul_f32_e64 v58, v137, v137
	v_mul_f32_e64 v59, v138, v138
	v_or_b32_dpp v76, v29, v29 wave_shr:1 row_mask:0xf bank_mask:0xf bound_ctrl:1
	v_add_f32_e64 v70, v138, v10
	v_pk_add_f32 v[38:39], v[38:39], v[40:41]
	v_or_b32_dpp v76, v29, v76 wave_shl:1 row_mask:0xf bank_mask:0xf bound_ctrl:1
	v_or3_b32 v17, v76, v89, v77
	v_or3_b32 v17, v17, v86, v87
	s_add_i32 s4, s34, 8
	s_cmpk_lt_u32 s4, 0x1ff
	s_cselect_b64 s[12:13], s[42:43], 0
	v_cmp_ne_u32_e64 s[30:31], 0, v17
	s_and_b64 s[30:31], s[30:31], s[12:13]
	v_cndmask_b32_e64 v17, 0, 1.0, s[30:31]
	v_pk_fma_f32 v[44:45], v[8:9], v[8:9], v[44:45] op_sel_hi:[0,1,1]
	v_pk_fma_f32 v[56:57], v[8:9], v[10:11], v[56:57] op_sel_hi:[1,0,1]
	v_fma_f32 v58, v9, v9, v58
	v_fma_f32 v59, v10, v10, v59
	v_add_f32_dpp v71, v17, v17 wave_shr:1 row_mask:0xf bank_mask:0xf bound_ctrl:1
	v_add_f32_e64 v70, v70, v42
	v_pk_fma_f32 v[44:45], v[40:41], v[40:41], v[44:45] op_sel_hi:[0,1,1]
	v_pk_fma_f32 v[56:57], v[40:41], v[42:43], v[56:57] op_sel_hi:[1,0,1]
	v_fma_f32 v58, v41, v41, v58
	v_fma_f32 v59, v42, v42, v59
	v_add_f32_dpp v71, v17, v71 wave_shl:1 row_mask:0xf bank_mask:0xf bound_ctrl:1
	v_pk_add_f32 v[84:85], v[64:65], v[38:39]
	v_pk_add_f32 v[90:91], v[6:7], v[84:85]
	v_pk_add_f32 v[6:7], v[78:79], v[44:45]
	v_pk_add_f32 v[64:65], v[20:21], v[6:7]
	v_pk_add_f32 v[20:21], v[96:97], v[56:57]
	v_pk_add_f32 v[78:79], v[46:47], v[20:21]
	v_pk_add_f32 v[96:97], v[102:103], v[58:59]
	v_pk_add_f32 v[46:47], v[50:51], v[96:97]
	v_pk_add_f32 v[50:51], v[106:107], v[70:71]
	v_pk_add_f32 v[100:101], v[52:53], v[50:51]
	v_mul_f32_e64 v112, v90, v22
	v_mul_f32_e64 v113, v91, v22
	v_mul_f32_e64 v114, v100, v22
	v_fma_f32 v17, v64, v22, v26
	v_mul_f32_e64 v29, v65, v22
	v_mul_f32_e64 v88, v78, v22
	v_fma_f32 v52, v46, v22, v26
	v_mul_f32_e64 v53, v79, v22
	v_fma_f32 v102, v47, v22, v26
	v_fma_f32 v17, -v112, v112, v17
	v_fma_f32 v29, -v112, v113, v29
	v_fma_f32 v88, -v112, v114, v88
	v_fma_f32 v52, -v113, v113, v52
	v_fma_f32 v53, -v113, v114, v53
	v_fma_f32 v102, -v114, v114, v102
	v_mul_f32_e64 v103, v53, v53
	v_mul_f32_e64 v106, v29, v102
	v_mul_f32_e64 v107, v88, v52
	v_mul_f32_e64 v124, v88, v88
	v_mul_f32_e64 v125, v17, v53
	v_mul_f32_e64 v126, v29, v29
	v_fma_f32 v103, v52, v102, -v103
	v_fma_f32 v106, v88, v53, -v106
	v_fma_f32 v107, v29, v53, -v107
	v_fma_f32 v124, v17, v102, -v124
	v_fma_f32 v125, v29, v88, -v125
	v_fma_f32 v126, v17, v52, -v126
	v_mul_f32_e64 v127, v17, v103
	v_fma_f32 v127, v29, v106, v127
	v_fma_f32 v127, v88, v107, v127
	v_rcp_f32_e32 v127, v127
	v_cmp_ne_u32_e64 vcc, s37, v25
	v_mul_f32_e64 v127, v127, v22
	v_cndmask_b32_e64 v127, 0, v127, s[30:31]
	v_cndmask_b32_e64 v17, 0, v18, vcc
	v_cndmask_b32_e64 v121, 0, v22, s[30:31]
	v_mul_f32_e64 v115, v103, v127
	v_mul_f32_e64 v116, v106, v127
	v_mul_f32_e64 v117, v107, v127
	v_mul_f32_e64 v118, v124, v127
	v_mul_f32_e64 v119, v125, v127
	v_mul_f32_e64 v120, v126, v127
	v_add_f32_e64 v122, v101, v17
	v_mov_b32_e32 v123, v25
	ds_write_b128 v23, v[112:115]
	ds_write_b128 v23, v[116:119] offset:1024
	ds_write_b128 v23, v[120:123] offset:2048
	v_mov_b32_dpp v46, v4 wave_shr:1 row_mask:0xf bank_mask:0xf bound_ctrl:1
	v_mov_b32_dpp v47, v5 wave_shr:1 row_mask:0xf bank_mask:0xf bound_ctrl:1
	v_mov_b32_dpp v78, v4 wave_shl:1 row_mask:0xf bank_mask:0xf bound_ctrl:1
	v_mov_b32_dpp v79, v5 wave_shl:1 row_mask:0xf bank_mask:0xf bound_ctrl:1
	v_pk_mul_f32 v[52:53], v[4:5], v[136:137] op_sel_hi:[1,0]
	v_pk_mul_f32 v[64:65], v[4:5], v[136:137] op_sel:[0,1]
	v_pk_mul_f32 v[100:101], v[4:5], v[138:139] op_sel_hi:[1,0]
	v_pk_add_f32 v[124:125], v[4:5], v[46:47]
	v_pk_fma_f32 v[52:53], v[46:47], v[8:9], v[52:53] op_sel_hi:[1,0,1]
	v_pk_fma_f32 v[64:65], v[46:47], v[8:9], v[64:65] op_sel:[0,1,0]
	v_pk_fma_f32 v[100:101], v[46:47], v[10:11], v[100:101] op_sel_hi:[1,0,1]
	v_pk_add_f32 v[124:125], v[124:125], v[78:79]
	v_pk_fma_f32 v[52:53], v[78:79], v[40:41], v[52:53] op_sel_hi:[1,0,1]
	v_pk_fma_f32 v[64:65], v[78:79], v[40:41], v[64:65] op_sel:[0,1,0]
	v_pk_fma_f32 v[100:101], v[78:79], v[42:43], v[100:101] op_sel_hi:[1,0,1]
	s_waitcnt lgkmcnt(0)
	s_barrier
	v_pk_add_f32 v[46:47], v[150:151], v[124:125]
	v_pk_add_f32 v[78:79], v[156:157], v[46:47]
	v_pk_add_f32 v[90:91], v[54:55], v[52:53]
	v_pk_add_f32 v[128:129], v[36:37], v[90:91]
	v_pk_add_f32 v[54:55], v[130:131], v[64:65]
	v_pk_add_f32 v[36:37], v[60:61], v[54:55]
	v_pk_add_f32 v[102:103], v[134:135], v[100:101]
	v_pk_add_f32 v[60:61], v[152:153], v[102:103]
	v_pk_fma_f32 v[128:129], v[112:113], v[78:79], v[128:129] op_sel_hi:[0,1,1] neg_lo:[1,0,0] neg_hi:[1,0,0]
	v_pk_fma_f32 v[36:37], v[112:113], v[78:79], v[36:37] op_sel:[1,0,0] neg_lo:[1,0,0] neg_hi:[1,0,0]
	v_pk_fma_f32 v[60:61], v[114:115], v[78:79], v[60:61] op_sel_hi:[0,1,1] neg_lo:[1,0,0] neg_hi:[1,0,0]
	v_pk_mul_f32 v[106:107], v[114:115], v[128:129] op_sel:[1,0]
	v_pk_mul_f32 v[126:127], v[116:117], v[128:129] op_sel_hi:[0,1]
	v_pk_mul_f32 v[130:131], v[116:117], v[128:129] op_sel:[1,0]
	v_pk_fma_f32 v[106:107], v[116:117], v[36:37], v[106:107] op_sel_hi:[0,1,1]
	v_pk_fma_f32 v[126:127], v[118:119], v[36:37], v[126:127] op_sel_hi:[0,1,1]
	v_pk_fma_f32 v[130:131], v[118:119], v[36:37], v[130:131] op_sel:[1,0,0]
	v_pk_fma_f32 v[106:107], v[116:117], v[60:61], v[106:107] op_sel:[1,0,0]
	v_pk_fma_f32 v[126:127], v[118:119], v[60:61], v[126:127] op_sel:[1,0,0]
	v_pk_fma_f32 v[130:131], v[120:121], v[60:61], v[130:131] op_sel_hi:[0,1,1]
	v_pk_mul_f32 v[132:133], v[112:113], v[106:107] op_sel_hi:[0,1]
	v_pk_fma_f32 v[132:133], v[112:113], v[126:127], v[132:133] op_sel:[1,0,0]
	v_pk_fma_f32 v[132:133], v[114:115], v[130:131], v[132:133] op_sel_hi:[0,1,1]
	v_pk_fma_f32 v[132:133], v[120:121], v[78:79], v[132:133] op_sel:[1,0,0] neg_lo:[0,0,1] neg_hi:[0,0,1]
	v_cmp_eq_u32_e64 s[10:11], 6, v123
	v_cmp_eq_u32_e64 s[14:15], 7, v123
	v_pk_add_f32 v[36:37], v[68:69], v[106:107]
	v_pk_add_f32 v[60:61], v[94:95], v[36:37]
	v_pk_add_f32 v[68:69], v[104:105], v[126:127]
	v_pk_add_f32 v[78:79], v[98:99], v[68:69]
	v_pk_add_f32 v[104:105], v[108:109], v[130:131]
	v_pk_add_f32 v[94:95], v[110:111], v[104:105]
	v_pk_add_f32 v[98:99], v[62:63], v[132:133]
	v_pk_add_f32 v[108:109], v[92:93], v[98:99]
	v_pk_fma_f32 v[92:93], v[12:13], v[60:61], v[108:109] op_sel_hi:[0,1,1]
	v_pk_fma_f32 v[128:129], v[80:81], v[60:61], v[108:109] op_sel_hi:[0,1,1]
	v_pk_fma_f32 v[92:93], v[12:13], v[78:79], v[92:93] op_sel:[1,0,0]
	v_pk_fma_f32 v[128:129], v[80:81], v[78:79], v[128:129] op_sel:[1,0,0]
	v_pk_fma_f32 v[92:93], v[14:15], v[94:95], v[92:93] op_sel_hi:[0,1,1]
	v_pk_fma_f32 v[128:129], v[82:83], v[94:95], v[128:129] op_sel_hi:[0,1,1]
	v_pk_fma_f32 v[108:109], v[140:141], v[60:61], v[108:109] op_sel_hi:[0,1,1]
	v_pk_fma_f32 v[108:109], v[140:141], v[78:79], v[108:109] op_sel:[1,0,0]
	v_pk_fma_f32 v[108:109], v[142:143], v[94:95], v[108:109] op_sel_hi:[0,1,1]
	v_cndmask_b32_e64 v62, 0, v18, s[10:11]
	v_cndmask_b32_e64 v63, 0, v18, s[14:15]
	v_add_f32_dpp v108, v92, v108 wave_shl:1 row_mask:0xf bank_mask:0xf bound_ctrl:1
	v_add_f32_dpp v109, v93, v109 wave_shl:1 row_mask:0xf bank_mask:0xf bound_ctrl:1
	s_add_i32 s4, s34, 8
	s_cmpk_lt_i32 s4, 0x201
	s_cselect_b64 s[12:13], s[0:1], 0
	v_add_f32_dpp v108, v128, v108 wave_shr:1 row_mask:0xf bank_mask:0xf bound_ctrl:1
	v_add_f32_dpp v109, v129, v109 wave_shr:1 row_mask:0xf bank_mask:0xf bound_ctrl:1
	v_pk_fma_f32 v[108:109], v[48:49], v[122:123], v[108:109] op_sel_hi:[1,0,1] neg_lo:[0,0,1] neg_hi:[0,0,1]
	v_pk_add_f32 v[108:109], v[108:109], v[62:63] neg_lo:[0,1] neg_hi:[0,1]
	v_pk_mul_f32 v[110:111], v[108:109], v[108:109]
	v_add_f32_e32 v110, v110, v111
	v_cndmask_b32_e64 v111, 0, v110, s[12:13]
	v_add_f32_e32 v1, v1, v111
	s_waitcnt vmcnt(0)
	v_mov_b32_dpp v12, v160 wave_shr:1 row_mask:0xf bank_mask:0xf bound_ctrl:1
	v_mov_b32_dpp v13, v161 wave_shr:1 row_mask:0xf bank_mask:0xf bound_ctrl:1
	v_mov_b32_dpp v14, v162 wave_shr:1 row_mask:0xf bank_mask:0xf bound_ctrl:1
	v_mov_b32_dpp v60, v160 wave_shl:1 row_mask:0xf bank_mask:0xf bound_ctrl:1
	v_mov_b32_dpp v61, v161 wave_shl:1 row_mask:0xf bank_mask:0xf bound_ctrl:1
	v_mov_b32_dpp v62, v162 wave_shl:1 row_mask:0xf bank_mask:0xf bound_ctrl:1
	s_add_i32 s4, s34, 12
	s_cmpk_lt_u32 s4, 0x201
	s_cselect_b64 s[12:13], s[40:41], 0
	v_cmp_eq_u32_e64 s[14:15], s37, v16
	s_and_b64 s[14:15], s[14:15], s[12:13]
	v_cndmask_b32_e64 v17, 0, 1, s[14:15]
	v_pk_add_f32 v[48:49], v[160:161], v[12:13]
	v_pk_mul_f32 v[78:79], v[160:161], v[160:161] op_sel_hi:[0,1]
	v_or_b32_dpp v25, v17, v17 wave_shr:1 row_mask:0xf bank_mask:0xf bound_ctrl:1
	v_pk_mul_f32 v[80:81], v[160:161], v[162:163] op_sel_hi:[1,0]
	v_or_b32_dpp v25, v17, v25 wave_shl:1 row_mask:0xf bank_mask:0xf bound_ctrl:1
	v_mul_f32_e64 v82, v161, v161
	v_mul_f32_e64 v83, v162, v162
	v_or_b32_dpp v29, v25, v25 wave_shr:1 row_mask:0xf bank_mask:0xf bound_ctrl:1
	v_add_f32_e64 v92, v162, v14
	v_pk_add_f32 v[48:49], v[48:49], v[60:61]
	v_or_b32_dpp v29, v25, v29 wave_shl:1 row_mask:0xf bank_mask:0xf bound_ctrl:1
	v_or3_b32 v17, v29, v76, v89
	v_or3_b32 v17, v17, v77, v86
	s_add_i32 s4, s34, 9
	s_cmpk_lt_u32 s4, 0x1ff
	s_cselect_b64 s[12:13], s[42:43], 0
	v_cmp_ne_u32_e64 s[30:31], 0, v17
	s_and_b64 s[30:31], s[30:31], s[12:13]
	v_cndmask_b32_e64 v17, 0, 1.0, s[30:31]
	v_pk_fma_f32 v[78:79], v[12:13], v[12:13], v[78:79] op_sel_hi:[0,1,1]
	v_pk_fma_f32 v[80:81], v[12:13], v[14:15], v[80:81] op_sel_hi:[1,0,1]
	v_fma_f32 v82, v13, v13, v82
	v_fma_f32 v83, v14, v14, v83
	v_add_f32_dpp v93, v17, v17 wave_shr:1 row_mask:0xf bank_mask:0xf bound_ctrl:1
	v_add_f32_e64 v92, v92, v62
	v_pk_fma_f32 v[78:79], v[60:61], v[60:61], v[78:79] op_sel_hi:[0,1,1]
	v_pk_fma_f32 v[80:81], v[60:61], v[62:63], v[80:81] op_sel_hi:[1,0,1]
	v_fma_f32 v82, v61, v61, v82
	v_fma_f32 v83, v62, v62, v83
	v_add_f32_dpp v93, v17, v93 wave_shl:1 row_mask:0xf bank_mask:0xf bound_ctrl:1
	v_pk_add_f32 v[94:95], v[84:85], v[48:49]
	v_pk_add_f32 v[84:85], v[6:7], v[78:79]
	v_pk_add_f32 v[6:7], v[20:21], v[80:81]
	v_pk_add_f32 v[20:21], v[96:97], v[82:83]
	v_pk_add_f32 v[96:97], v[50:51], v[92:93]
	v_mul_f32_e64 v108, v94, v22
	v_mul_f32_e64 v109, v95, v22
	v_mul_f32_e64 v110, v96, v22
	v_fma_f32 v17, v84, v22, v26
	v_mul_f32_e64 v25, v85, v22
	v_mul_f32_e64 v87, v6, v22
	v_fma_f32 v88, v20, v22, v26
	v_mul_f32_e64 v50, v7, v22
	v_fma_f32 v51, v21, v22, v26
	v_fma_f32 v17, -v108, v108, v17
	v_fma_f32 v25, -v108, v109, v25
	v_fma_f32 v87, -v108, v110, v87
	v_fma_f32 v88, -v109, v109, v88
	v_fma_f32 v50, -v109, v110, v50
	v_fma_f32 v51, -v110, v110, v51
	v_mul_f32_e64 v120, v50, v50
	v_mul_f32_e64 v121, v25, v51
	v_mul_f32_e64 v122, v87, v88
	v_mul_f32_e64 v123, v87, v87
	v_mul_f32_e64 v128, v17, v50
	v_mul_f32_e64 v129, v25, v25
	v_fma_f32 v120, v88, v51, -v120
	v_fma_f32 v121, v87, v50, -v121
	v_fma_f32 v122, v25, v50, -v122
	v_fma_f32 v123, v17, v51, -v123
	v_fma_f32 v128, v25, v87, -v128
	v_fma_f32 v129, v17, v88, -v129
	v_mul_f32_e64 v134, v17, v120
	v_fma_f32 v134, v25, v121, v134
	v_fma_f32 v134, v87, v122, v134
	v_rcp_f32_e32 v134, v134
	v_cmp_ne_u32_e64 vcc, s37, v24
	v_mul_f32_e64 v134, v134, v22
	v_cndmask_b32_e64 v134, 0, v134, s[30:31]
	v_cndmask_b32_e64 v17, 0, v18, vcc
	v_cndmask_b32_e64 v117, 0, v22, s[30:31]
	v_mul_f32_e64 v111, v120, v134
	v_mul_f32_e64 v112, v121, v134
	v_mul_f32_e64 v113, v122, v134
	v_mul_f32_e64 v114, v123, v134
	v_mul_f32_e64 v115, v128, v134
	v_mul_f32_e64 v116, v129, v134
	v_add_f32_e64 v118, v97, v17
	v_mov_b32_e32 v119, v24
	ds_write_b128 v23, v[108:111] offset:3072
	ds_write_b128 v23, v[112:115] offset:4096
	ds_write_b128 v23, v[116:119] offset:5120
	v_mov_b32_dpp v20, v66 wave_shr:1 row_mask:0xf bank_mask:0xf bound_ctrl:1
	v_mov_b32_dpp v21, v67 wave_shr:1 row_mask:0xf bank_mask:0xf bound_ctrl:1
	v_mov_b32_dpp v24, v66 wave_shl:1 row_mask:0xf bank_mask:0xf bound_ctrl:1
	v_mov_b32_dpp v25, v67 wave_shl:1 row_mask:0xf bank_mask:0xf bound_ctrl:1
	v_pk_mul_f32 v[6:7], v[66:67], v[160:161] op_sel_hi:[1,0]
	v_pk_mul_f32 v[50:51], v[66:67], v[160:161] op_sel:[0,1]
	v_pk_mul_f32 v[86:87], v[66:67], v[162:163] op_sel_hi:[1,0]
	v_pk_add_f32 v[94:95], v[66:67], v[20:21]
	v_pk_fma_f32 v[6:7], v[20:21], v[12:13], v[6:7] op_sel_hi:[1,0,1]
	v_pk_fma_f32 v[50:51], v[20:21], v[12:13], v[50:51] op_sel:[0,1,0]
	v_pk_fma_f32 v[86:87], v[20:21], v[14:15], v[86:87] op_sel_hi:[1,0,1]
	v_pk_add_f32 v[94:95], v[94:95], v[24:25]
	v_pk_fma_f32 v[6:7], v[24:25], v[60:61], v[6:7] op_sel_hi:[1,0,1]
	v_pk_fma_f32 v[50:51], v[24:25], v[60:61], v[50:51] op_sel:[0,1,0]
	v_pk_fma_f32 v[86:87], v[24:25], v[62:63], v[86:87] op_sel_hi:[1,0,1]
	s_waitcnt lgkmcnt(0)
	s_barrier
	v_pk_add_f32 v[20:21], v[46:47], v[94:95]
	v_pk_add_f32 v[46:47], v[90:91], v[6:7]
	v_pk_add_f32 v[90:91], v[54:55], v[50:51]
	v_pk_add_f32 v[54:55], v[102:103], v[86:87]
	v_pk_fma_f32 v[46:47], v[108:109], v[20:21], v[46:47] op_sel_hi:[0,1,1] neg_lo:[1,0,0] neg_hi:[1,0,0]
	v_pk_fma_f32 v[90:91], v[108:109], v[20:21], v[90:91] op_sel:[1,0,0] neg_lo:[1,0,0] neg_hi:[1,0,0]
	v_pk_fma_f32 v[54:55], v[110:111], v[20:21], v[54:55] op_sel_hi:[0,1,1] neg_lo:[1,0,0] neg_hi:[1,0,0]
	v_pk_mul_f32 v[24:25], v[110:111], v[46:47] op_sel:[1,0]
	v_pk_mul_f32 v[84:85], v[112:113], v[46:47] op_sel_hi:[0,1]
	v_pk_mul_f32 v[96:97], v[112:113], v[46:47] op_sel:[1,0]
	v_pk_fma_f32 v[24:25], v[112:113], v[90:91], v[24:25] op_sel_hi:[0,1,1]
	v_pk_fma_f32 v[84:85], v[114:115], v[90:91], v[84:85] op_sel_hi:[0,1,1]
	v_pk_fma_f32 v[96:97], v[114:115], v[90:91], v[96:97] op_sel:[1,0,0]
	v_pk_fma_f32 v[24:25], v[112:113], v[54:55], v[24:25] op_sel:[1,0,0]
	v_pk_fma_f32 v[84:85], v[114:115], v[54:55], v[84:85] op_sel:[1,0,0]
	v_pk_fma_f32 v[96:97], v[116:117], v[54:55], v[96:97] op_sel_hi:[0,1,1]
	v_pk_mul_f32 v[102:103], v[108:109], v[24:25] op_sel_hi:[0,1]
	v_pk_fma_f32 v[102:103], v[108:109], v[84:85], v[102:103] op_sel:[1,0,0]
	v_pk_fma_f32 v[102:103], v[110:111], v[96:97], v[102:103] op_sel_hi:[0,1,1]
	v_pk_fma_f32 v[102:103], v[116:117], v[20:21], v[102:103] op_sel:[1,0,0] neg_lo:[0,0,1] neg_hi:[0,0,1]
	v_cmp_eq_u32_e64 s[10:11], 6, v119
	v_cmp_eq_u32_e64 s[14:15], 7, v119
	v_pk_add_f32 v[20:21], v[36:37], v[24:25]
	v_pk_add_f32 v[36:37], v[68:69], v[84:85]
	v_pk_add_f32 v[46:47], v[104:105], v[96:97]
	v_pk_add_f32 v[54:55], v[98:99], v[102:103]
	v_pk_fma_f32 v[90:91], v[32:33], v[20:21], v[54:55] op_sel_hi:[0,1,1]
	v_pk_fma_f32 v[98:99], v[72:73], v[20:21], v[54:55] op_sel_hi:[0,1,1]
	v_pk_fma_f32 v[90:91], v[32:33], v[36:37], v[90:91] op_sel:[1,0,0]
	v_pk_fma_f32 v[98:99], v[72:73], v[36:37], v[98:99] op_sel:[1,0,0]
	v_pk_fma_f32 v[90:91], v[34:35], v[46:47], v[90:91] op_sel_hi:[0,1,1]
	v_pk_fma_f32 v[98:99], v[74:75], v[46:47], v[98:99] op_sel_hi:[0,1,1]
	v_pk_fma_f32 v[54:55], v[144:145], v[20:21], v[54:55] op_sel_hi:[0,1,1]
	v_pk_fma_f32 v[54:55], v[144:145], v[36:37], v[54:55] op_sel:[1,0,0]
	v_pk_fma_f32 v[54:55], v[146:147], v[46:47], v[54:55] op_sel_hi:[0,1,1]
	v_cndmask_b32_e64 v68, 0, v18, s[10:11]
	v_cndmask_b32_e64 v69, 0, v18, s[14:15]
	v_add_f32_dpp v54, v90, v54 wave_shl:1 row_mask:0xf bank_mask:0xf bound_ctrl:1
	v_add_f32_dpp v55, v91, v55 wave_shl:1 row_mask:0xf bank_mask:0xf bound_ctrl:1
	s_add_i32 s4, s34, 9
	s_cmpk_lt_i32 s4, 0x201
	s_cselect_b64 s[12:13], s[0:1], 0
	v_add_f32_dpp v54, v98, v54 wave_shr:1 row_mask:0xf bank_mask:0xf bound_ctrl:1
	v_add_f32_dpp v55, v99, v55 wave_shr:1 row_mask:0xf bank_mask:0xf bound_ctrl:1
	v_pk_fma_f32 v[54:55], v[30:31], v[118:119], v[54:55] op_sel_hi:[1,0,1] neg_lo:[0,0,1] neg_hi:[0,0,1]
	v_pk_add_f32 v[54:55], v[54:55], v[68:69] neg_lo:[0,1] neg_hi:[0,1]
	v_pk_mul_f32 v[104:105], v[54:55], v[54:55]
	v_add_f32_e32 v104, v104, v105
	v_cndmask_b32_e64 v105, 0, v104, s[12:13]
	v_add_f32_e32 v1, v1, v105
	v_mov_b32_e32 v0, v1
	s_branch .LBB0_29
